# c30: c29 + attention tile loops prefetch next tile's bias/K fragments from LDS during the current tile's softmax (P bf16/V fragments moved to spare VGPRs)
# baseline (speedup 1.0000x reference)
; #define GAS __attribute__((address_space(1)))
; #define LAS __attribute__((address_space(3)))
; __device__ __forceinline__ void issue_loads(const UnitP& P, StageRegs& R, int tid) {
;     ...
;     const long qtok = (long)(P.mq0 + 32 * wave + r32) * P.dil + P.res;
; #pragma unroll
;     for (int s = 0; s < 4; ++s) R.q[s] = *(const GAS bf16x8*)(P.qg + qtok * P.qpitch + hi * 8 + 16 * s);
; template <bool BAND, int OUTMODE>
; __device__ __forceinline__ void compute(LAS unsigned char* lds, const bf16x8 (&qr)[4], int tid, int mq0, int dil, int res, int kt_min, int bias_tab, float sink2,
;                                         bf16* ob, int opitch, float* lsep) {
;     const int lane = tid & 63, wave = __builtin_amdgcn_readfirstlane(tid >> 6), r32 = lane & 31, hi = lane >> 5;
;     constexpr int NT = BAND ? 5 : 8;
;     const int kt0 = BAND ? wave : 0;
;     int t0 = BAND ? kt_min - kt0 : 0; t0 = t0 < 0 ? 0 : t0;
;     const LAS unsigned char* kb = lds + K_OFF + (32 * kt0 + r32) * KSTR + hi * 16;
;     const LAS float* bl = (const LAS float*)(lds + B_OFF) + bias_tab * BT_FLOATS + (31 - r32 + 4 * hi);
;     const int i16 = lane & 15, q4 = i16 >> 2, p4 = i16 & 3, blk16 = (lane >> 4) & 1;
;     const LAS unsigned char* vb = lds + V_OFF + (32 * kt0 + 4 * hi + q4) * 64 + blk16 * 32 + p4 * 8;
;     float mref = -1e20f, l = 0.f;
;     f32x16 o0, o1;
; #pragma unroll
;     for (int i = 0; i < 16; ++i) { o0[i] = 0.f; o1[i] = 0.f; }
.LBB0_370:
	s_or_b64 exec, exec, s[24:25]
	s_lshl_b32 s12, s14, 6
	s_ashr_i32 s13, s12, 31
	s_lshl_b64 s[22:23], s[12:13], 1
	s_add_u32 s22, s15, s22
	s_addc_u32 s23, s39, s23
	s_add_i32 s0, s30, 11
	v_add_u32_e32 v3, s31, v152
	v_mov_b64_e32 v[4:5], s[22:23]
	s_cmp_lt_u32 s0, 23
	v_mad_i64_i32 v[4:5], s[22:23], v3, s5, v[4:5]
	v_mov_b32_e32 v3, v137
	s_cselect_b32 s0, 4, 0
	s_ashr_i32 s19, s18, 31
	v_lshl_add_u64 v[4:5], v[4:5], 0, v[2:3]
	s_lshl_b64 s[22:23], s[18:19], 2
	global_load_dwordx4 v[60:63], v[4:5], off
	global_load_dwordx4 v[74:77], v[4:5], off offset:32
	global_load_dwordx4 v[78:81], v[4:5], off offset:64
	global_load_dwordx4 v[82:85], v[4:5], off offset:96
	s_add_u32 s22, s36, s22
	s_addc_u32 s23, s37, s23
	global_load_dword v135, v137, s[22:23]
	v_readfirstlane_b32 s1, v0
	v_bfe_u32 v145, v0, 5, 1
	s_lshr_b32 s1, s1, 6
	v_lshlrev_b32_e32 v156, 2, v145
	v_and_b32_e32 v157, 3, v45
	v_lshlrev_b32_e32 v5, 1, v0
	s_lshl_b32 s5, s1, 5
	v_and_b32_e32 v146, 32, v5
	s_sub_i32 s0, s0, s1
	v_or3_b32 v5, s5, v156, v157
	s_max_i32 s0, s0, 0
	v_lshlrev_b32_e32 v5, 6, v5
	s_mul_i32 s19, s18, 0x300
	s_add_i32 s18, s0, -1
	v_lshl_add_u32 v5, s0, 11, v5
	s_mul_i32 s22, s0, 0x1200
	s_lshl_b32 s0, s0, 7
	v_lshlrev_b32_e32 v134, 4, v145
	v_xor_b32_e32 v4, 31, v164
	v_and_b32_e32 v147, 24, v44
	s_add_i32 s19, s19, s0
	v_or3_b32 v159, v5, v146, v147
	s_mulk_i32 s1, 0x1200
	v_or_b32_e32 v5, s19, v134
	v_lshlrev_b32_e32 v165, 2, v4
	v_mov_b32_e32 v18, v137
	v_mov_b32_e32 v19, v137
	s_add_i32 s22, s22, s1
	v_mul_u32_u24_e32 v160, 0x90, v164
	v_add_u32_e32 v166, v5, v165
	v_mov_b32_e32 v4, v137
	v_mov_b32_e32 v5, v137
	v_mov_b32_e32 v6, v137
	v_mov_b32_e32 v7, v137
	v_mov_b32_e32 v8, v137
	v_mov_b32_e32 v9, v137
	v_mov_b32_e32 v10, v137
	v_mov_b32_e32 v11, v137
	v_mov_b32_e32 v12, v137
	v_mov_b32_e32 v13, v137
	v_mov_b32_e32 v14, v137
	v_mov_b32_e32 v15, v137
	v_mov_b32_e32 v16, v137
	v_mov_b32_e32 v17, v137
	v_mov_b64_e32 v[34:35], v[18:19]
	v_mul_u32_u24_e32 v158, 0x90, v149
	v_mul_u32_u24_e32 v73, 0x90, v150
	v_mul_u32_u24_e32 v3, 0x90, v148
	v_add3_u32 v161, s22, v160, v134
	v_mov_b32_e32 v167, 0xe0ad78ec
	v_mov_b64_e32 v[32:33], v[16:17]
	v_mov_b64_e32 v[30:31], v[14:15]
	v_mov_b64_e32 v[28:29], v[12:13]
	v_mov_b64_e32 v[26:27], v[10:11]
	v_mov_b64_e32 v[24:25], v[8:9]
	v_mov_b64_e32 v[22:23], v[6:7]
	v_mov_b64_e32 v[20:21], v[4:5]
	v_add_u32_e32 v244, 0x19800, v166
	ds_read2_b32 v[36:37], v244 offset1:1
	ds_read2_b32 v[38:39], v244 offset0:2 offset1:3
	ds_read2_b32 v[40:41], v244 offset0:8 offset1:9
	ds_read2_b32 v[42:43], v244 offset0:10 offset1:11
	v_add_u32_e32 v246, 0, v161
	ds_read_b128 v[236:239], v246
	ds_read2_b32 v[44:45], v244 offset0:16 offset1:17
	ds_read2_b32 v[46:47], v244 offset0:18 offset1:19
	ds_read2_b32 v[48:49], v244 offset0:24 offset1:25
	ds_read2_b32 v[50:51], v244 offset0:26 offset1:27
	ds_read_b128 v[240:243], v246 offset:32
	s_branch .LBB0_372
; #define LAS __attribute__((address_space(3)))
; template <bool BAND, int OUTMODE>
; __device__ __forceinline__ void compute(LAS unsigned char* lds, const bf16x8 (&qr)[4], int tid, int mq0, int dil, int res, int kt_min, int bias_tab, float sink2,
;                                         bf16* ob, int opitch, float* lsep) {
;     ...
;     for (int t = t0; t < NT; ++t) {
;         f32x16 S;
;         if (BAND) {
; #pragma unroll
;             for (int i = 0; i < 16; ++i) S[i] = bl[32 * t + (i & 3) + 8 * (i >> 2)];
;         } else {
; #pragma unroll
;             for (int i = 0; i < 16; ++i) S[i] = 0.f;
;         }
; #pragma unroll
;         for (int s = 0; s < 4; ++s) { const bf16x8 kf = *(const LAS bf16x8*)(kb + t * 32 * KSTR + s * 32); S = __builtin_amdgcn_mfma_f32_32x32x16_bf16(kf, qr[s], S, 0, 0, 0); }
;         float m0 = fmaxf(fmaxf(S[0], S[1]), fmaxf(S[2], S[3])), m1 = fmaxf(fmaxf(S[4], S[5]), fmaxf(S[6], S[7])), m2 = fmaxf(fmaxf(S[8], S[9]), fmaxf(S[10], S[11])), m3 = fmaxf(fmaxf(S[12], S[13]), fmaxf(S[14], S[15]));
;         const float mt = xhalf_max(fmaxf(fmaxf(m0, m1), fmaxf(m2, m3)));
;         if (__any(mt > mref + THR)) {
;             const float mnew = fmaxf(mref, mt), f = __builtin_amdgcn_exp2f(mref - mnew);
;             mref = mnew; l *= f;
; #pragma unroll
;             for (int i = 0; i < 16; ++i) { o0[i] *= f; o1[i] *= f; }
;         }
; #pragma unroll
;         for (int i = 0; i < 16; ++i) { const float p = __builtin_amdgcn_exp2f(S[i] - mref); S[i] = p; l += p; }
; #pragma unroll
;         for (int s = 0; s < 2; ++s) {
;             v4u pw; pw.x = cvtpk(S[8 * s + 0], S[8 * s + 1]); pw.y = cvtpk(S[8 * s + 2], S[8 * s + 3]); pw.z = cvtpk(S[8 * s + 4], S[8 * s + 5]); pw.w = cvtpk(S[8 * s + 6], S[8 * s + 7]);
;             const bf16x8 pa = __builtin_bit_cast(bf16x8, pw);
;             const LAS unsigned char* vp = vb + (32 * t + 16 * s) * 64;
;             const s16x4 a0 = vtr(vp), a1 = vtr(vp + 8 * 64), b0 = vtr(vp + VPLANE), b1 = vtr(vp + VPLANE + 8 * 64);
;             const bf16x8 v0 = __builtin_shufflevector(a0, a1, 0, 1, 2, 3, 4, 5, 6, 7), v1 = __builtin_shufflevector(b0, b1, 0, 1, 2, 3, 4, 5, 6, 7);
;             o0 = __builtin_amdgcn_mfma_f32_32x32x16_bf16(v0, pa, o0, 0, 0, 0);
;             o1 = __builtin_amdgcn_mfma_f32_32x32x16_bf16(v1, pa, o1, 0, 0, 0);
;         }
;     }
.LBB0_371:
	v_pk_add_f32 v[220:221], v[36:37], v[166:167] op_sel:[0,1] op_sel_hi:[1,1] neg_lo:[0,1] neg_hi:[0,1]
	v_pk_add_f32 v[222:223], v[38:39], v[166:167] op_sel:[0,1] op_sel_hi:[1,1] neg_lo:[0,1] neg_hi:[0,1]
	v_pk_add_f32 v[224:225], v[40:41], v[166:167] op_sel:[0,1] op_sel_hi:[1,1] neg_lo:[0,1] neg_hi:[0,1]
	v_pk_add_f32 v[226:227], v[42:43], v[166:167] op_sel:[0,1] op_sel_hi:[1,1] neg_lo:[0,1] neg_hi:[0,1]
	v_pk_add_f32 v[228:229], v[44:45], v[166:167] op_sel:[0,1] op_sel_hi:[1,1] neg_lo:[0,1] neg_hi:[0,1]
	v_pk_add_f32 v[230:231], v[46:47], v[166:167] op_sel:[0,1] op_sel_hi:[1,1] neg_lo:[0,1] neg_hi:[0,1]
	v_pk_add_f32 v[232:233], v[48:49], v[166:167] op_sel:[0,1] op_sel_hi:[1,1] neg_lo:[0,1] neg_hi:[0,1]
	v_pk_add_f32 v[234:235], v[50:51], v[166:167] op_sel:[0,1] op_sel_hi:[1,1] neg_lo:[0,1] neg_hi:[0,1]
	v_add_u32_e32 v161, 0x1200, v161
	v_add_u32_e32 v166, 0x80, v166
	v_add_u32_e32 v244, 0x19800, v166
	ds_read2_b32 v[36:37], v244 offset1:1
	ds_read2_b32 v[38:39], v244 offset0:2 offset1:3
	ds_read2_b32 v[40:41], v244 offset0:8 offset1:9
	ds_read2_b32 v[42:43], v244 offset0:10 offset1:11
	v_add_u32_e32 v246, 0, v161
	ds_read_b128 v[236:239], v246
	ds_read2_b32 v[44:45], v244 offset0:16 offset1:17
	ds_read2_b32 v[46:47], v244 offset0:18 offset1:19
	ds_read2_b32 v[48:49], v244 offset0:24 offset1:25
	ds_read2_b32 v[50:51], v244 offset0:26 offset1:27
	ds_read_b128 v[240:243], v246 offset:32
	v_exp_f32_e32 v200, v220
	v_exp_f32_e32 v201, v221
	v_exp_f32_e32 v202, v222
	v_exp_f32_e32 v203, v223
	v_exp_f32_e32 v204, v224
	v_exp_f32_e32 v205, v225
	v_exp_f32_e32 v206, v226
	v_exp_f32_e32 v207, v227
	v_add_u32_e32 v184, 0, v159
	v_exp_f32_e32 v208, v228
	ds_read_b64_tr_b16 v[190:191], v184 offset:55296
	ds_read_b64_tr_b16 v[192:193], v184 offset:55808
	v_exp_f32_e32 v209, v229
	v_add_u32_e32 v245, 0x6000, v184
	v_exp_f32_e32 v210, v230
	ds_read_b64_tr_b16 v[194:195], v245 offset:55296
	ds_read_b64_tr_b16 v[196:197], v245 offset:55808
	ds_read_b64_tr_b16 v[168:169], v184 offset:56320
	ds_read_b64_tr_b16 v[170:171], v184 offset:56832
	v_exp_f32_e32 v211, v231
	v_exp_f32_e32 v212, v232
	v_cvt_pk_bf16_f32 v186, v200, v201
	v_cvt_pk_bf16_f32 v187, v202, v203
	v_cvt_pk_bf16_f32 v188, v204, v205
	v_cvt_pk_bf16_f32 v189, v206, v207
	s_add_i32 s18, s18, 1
	s_waitcnt lgkmcnt(4)
	v_mfma_f32_32x32x16_bf16 v[20:35], v[190:193], v[186:189], v[20:35]
	v_exp_f32_e32 v213, v233
	ds_read_b64_tr_b16 v[190:191], v245 offset:56320
	ds_read_b64_tr_b16 v[192:193], v245 offset:56832
	v_add_u32_e32 v159, 0x800, v159
	s_waitcnt lgkmcnt(4)
	v_mfma_f32_32x32x16_bf16 v[4:19], v[194:197], v[186:189], v[4:19]
	v_exp_f32_e32 v214, v234
	v_exp_f32_e32 v215, v235
	v_cvt_pk_bf16_f32 v186, v208, v209
	v_cvt_pk_bf16_f32 v187, v210, v211
	v_cvt_pk_bf16_f32 v188, v212, v213
	v_cvt_pk_bf16_f32 v189, v214, v215
	s_cmp_lt_u32 s18, 4
	s_waitcnt lgkmcnt(2)
	v_mfma_f32_32x32x16_bf16 v[20:35], v[168:171], v[186:189], v[20:35]
	s_waitcnt lgkmcnt(0)
	v_mfma_f32_32x32x16_bf16 v[4:19], v[190:193], v[186:189], v[4:19]
	v_pk_add_f32 v[220:221], v[200:201], v[202:203]
	v_pk_add_f32 v[222:223], v[204:205], v[206:207]
	v_pk_add_f32 v[224:225], v[208:209], v[210:211]
	v_pk_add_f32 v[226:227], v[212:213], v[214:215]
	v_pk_add_f32 v[220:221], v[220:221], v[222:223]
	v_pk_add_f32 v[224:225], v[224:225], v[226:227]
	v_pk_add_f32 v[220:221], v[220:221], v[224:225]
	v_add_f32_e32 v220, v220, v221
	v_add_f32_e32 v137, v137, v220
	s_cbranch_scc0 .LBB0_374
.LBB0_372:
	v_add_u32_e32 v176, 0, v161
	s_waitcnt vmcnt(18) lgkmcnt(1)
	v_mfma_f32_32x32x16_bf16 v[36:51], v[236:239], v[118:121], v[36:51]
	s_waitcnt vmcnt(17) lgkmcnt(0)
	v_mfma_f32_32x32x16_bf16 v[36:51], v[240:243], v[122:125], v[36:51]
	ds_read_b128 v[168:171], v176 offset:64
	ds_read_b128 v[172:175], v176 offset:96
	s_waitcnt vmcnt(16) lgkmcnt(1)
	v_mfma_f32_32x32x16_bf16 v[36:51], v[168:171], v[126:129], v[36:51]
	s_waitcnt vmcnt(15) lgkmcnt(0)
	v_mfma_f32_32x32x16_bf16 v[36:51], v[172:175], v[130:133], v[36:51]
	s_nop 11
	v_max3_f32 v168, v36, v37, v38
	v_max3_f32 v169, v39, v40, v41
	v_max3_f32 v170, v42, v43, v44
	v_max3_f32 v171, v45, v46, v47
	v_max3_f32 v172, v48, v49, v50
	v_max3_f32 v168, v168, v169, v51
	v_max3_f32 v170, v170, v171, v172
	v_max_f32_e32 v168, v168, v170
	v_mov_b32_e32 v169, v168
	s_nop 1
	v_permlane32_swap_b32_e32 v168, v169
	v_max_f32_e32 v168, v168, v169
	v_add_f32_e32 v169, 0x41000000, v167
	v_cmp_gt_f32_e32 vcc, v168, v169
	s_cbranch_vccz .LBB0_371
	v_max_f32_e32 v168, v168, v168
	v_max_f32_e32 v169, v167, v167
	v_max_f32_e32 v169, v169, v168
	v_sub_f32_e32 v167, v167, v169
	v_exp_f32_e32 v168, v167
	v_mov_b32_e32 v167, v169
	v_pk_mul_f32 v[34:35], v[34:35], v[168:169] op_sel_hi:[1,0]
	v_pk_mul_f32 v[32:33], v[32:33], v[168:169] op_sel_hi:[1,0]
	v_pk_mul_f32 v[30:31], v[30:31], v[168:169] op_sel_hi:[1,0]
	v_pk_mul_f32 v[28:29], v[28:29], v[168:169] op_sel_hi:[1,0]
	v_pk_mul_f32 v[26:27], v[26:27], v[168:169] op_sel_hi:[1,0]
	v_pk_mul_f32 v[24:25], v[24:25], v[168:169] op_sel_hi:[1,0]
	v_pk_mul_f32 v[22:23], v[22:23], v[168:169] op_sel_hi:[1,0]
	v_pk_mul_f32 v[20:21], v[20:21], v[168:169] op_sel_hi:[1,0]
	v_pk_mul_f32 v[18:19], v[18:19], v[168:169] op_sel_hi:[1,0]
	v_pk_mul_f32 v[16:17], v[16:17], v[168:169] op_sel_hi:[1,0]
	v_pk_mul_f32 v[14:15], v[14:15], v[168:169] op_sel_hi:[1,0]
	v_pk_mul_f32 v[12:13], v[12:13], v[168:169] op_sel_hi:[1,0]
	v_pk_mul_f32 v[10:11], v[10:11], v[168:169] op_sel_hi:[1,0]
	v_pk_mul_f32 v[8:9], v[8:9], v[168:169] op_sel_hi:[1,0]
	v_pk_mul_f32 v[6:7], v[6:7], v[168:169] op_sel_hi:[1,0]
	v_pk_mul_f32 v[4:5], v[4:5], v[168:169] op_sel_hi:[1,0]
	v_mul_f32_e32 v137, v137, v168
	s_branch .LBB0_371

; #define GAS __attribute__((address_space(1)))
; #define LAS __attribute__((address_space(3)))
; __device__ __forceinline__ void issue_loads(const UnitP& P, StageRegs& R, int tid) {
;     ...
;     const long qtok = (long)(P.mq0 + 32 * wave + r32) * P.dil + P.res;
; #pragma unroll
;     for (int s = 0; s < 4; ++s) R.q[s] = *(const GAS bf16x8*)(P.qg + qtok * P.qpitch + hi * 8 + 16 * s);
; template <bool BAND, int OUTMODE>
; __device__ __forceinline__ void compute(LAS unsigned char* lds, const bf16x8 (&qr)[4], int tid, int mq0, int dil, int res, int kt_min, int bias_tab, float sink2,
;                                         bf16* ob, int opitch, float* lsep) {
;     const int lane = tid & 63, wave = __builtin_amdgcn_readfirstlane(tid >> 6), r32 = lane & 31, hi = lane >> 5;
;     constexpr int NT = BAND ? 5 : 8;
;     const int kt0 = BAND ? wave : 0;
;     int t0 = BAND ? kt_min - kt0 : 0; t0 = t0 < 0 ? 0 : t0;
;     const LAS unsigned char* kb = lds + K_OFF + (32 * kt0 + r32) * KSTR + hi * 16;
;     const LAS float* bl = (const LAS float*)(lds + B_OFF) + bias_tab * BT_FLOATS + (31 - r32 + 4 * hi);
;     const int i16 = lane & 15, q4 = i16 >> 2, p4 = i16 & 3, blk16 = (lane >> 4) & 1;
;     const LAS unsigned char* vb = lds + V_OFF + (32 * kt0 + 4 * hi + q4) * 64 + blk16 * 32 + p4 * 8;
;     float mref = -1e20f, l = 0.f;
;     f32x16 o0, o1;
; #pragma unroll
;     for (int i = 0; i < 16; ++i) { o0[i] = 0.f; o1[i] = 0.f; }
.LBB0_378:
	s_or_b64 exec, exec, s[22:23]
	s_lshl_b32 s6, s43, 6
	s_ashr_i32 s7, s6, 31
	s_lshl_b64 s[6:7], s[6:7], 1
	s_add_u32 s6, s15, s6
	s_addc_u32 s7, s39, s7
	s_add_i32 s0, s30, 12
	v_add_u32_e32 v3, s38, v152
	v_mov_b64_e32 v[4:5], s[6:7]
	s_cmp_lt_u32 s0, 23
	v_mad_i64_i32 v[4:5], s[6:7], v3, s3, v[4:5]
	v_mov_b32_e32 v3, 0
	s_cselect_b32 s0, 4, 0
	s_ashr_i32 s15, s14, 31
	v_lshl_add_u64 v[4:5], v[4:5], 0, v[2:3]
	s_lshl_b64 s[6:7], s[14:15], 2
	global_load_dwordx4 v[86:89], v[4:5], off
	global_load_dwordx4 v[90:93], v[4:5], off offset:32
	global_load_dwordx4 v[94:97], v[4:5], off offset:64
	global_load_dwordx4 v[98:101], v[4:5], off offset:96
	s_add_u32 s6, s36, s6
	s_addc_u32 s7, s37, s7
	global_load_dword v65, v3, s[6:7]
	v_readfirstlane_b32 s1, v0
	s_lshr_b32 s1, s1, 6
	s_lshl_b32 s3, s1, 5
	s_sub_i32 s0, s0, s1
	s_max_i32 s0, s0, 0
	v_or_b32_e32 v4, s3, v156
	v_add_lshl_u32 v4, v4, v157, 6
	s_mul_i32 s7, s0, 0x1200
	s_mulk_i32 s1, 0x1200
	s_add_i32 s6, s0, -1
	v_lshl_add_u32 v4, s0, 11, v4
	s_add_i32 s7, s7, s1
	s_mul_i32 s1, s40, 0x300
	s_lshl_b32 s0, s0, 7
	v_or_b32_e32 v4, v4, v146
	s_add_i32 s1, s1, s0
	v_add_u32_e32 v135, v4, v147
	v_or_b32_e32 v4, s1, v134
	v_add_u32_e32 v4, v4, v165
	s_mulk_i32 s41, 0x2400
	v_mov_b32_e32 v18, v3
	v_mov_b32_e32 v19, v3
	v_subrev_u32_e32 v138, s41, v4
	v_mov_b32_e32 v4, v3
	v_mov_b32_e32 v5, v3
	v_mov_b32_e32 v6, v3
	v_mov_b32_e32 v7, v3
	v_mov_b32_e32 v8, v3
	v_mov_b32_e32 v9, v3
	v_mov_b32_e32 v10, v3
	v_mov_b32_e32 v11, v3
	v_mov_b32_e32 v12, v3
	v_mov_b32_e32 v13, v3
	v_mov_b32_e32 v14, v3
	v_mov_b32_e32 v15, v3
	v_mov_b32_e32 v16, v3
	v_mov_b32_e32 v17, v3
	v_mov_b64_e32 v[34:35], v[18:19]
	v_add3_u32 v137, s7, v160, v134
	v_mov_b32_e32 v139, 0xe0ad78ec
	v_mov_b64_e32 v[32:33], v[16:17]
	v_mov_b64_e32 v[30:31], v[14:15]
	v_mov_b64_e32 v[28:29], v[12:13]
	v_mov_b64_e32 v[26:27], v[10:11]
	v_mov_b64_e32 v[24:25], v[8:9]
	v_mov_b64_e32 v[22:23], v[6:7]
	v_mov_b64_e32 v[20:21], v[4:5]
	v_add_u32_e32 v244, 0x19800, v138
	ds_read2_b32 v[36:37], v244 offset1:1
	ds_read2_b32 v[38:39], v244 offset0:2 offset1:3
	ds_read2_b32 v[40:41], v244 offset0:8 offset1:9
	ds_read2_b32 v[42:43], v244 offset0:10 offset1:11
	v_add_u32_e32 v246, 0, v137
	ds_read_b128 v[236:239], v246
	ds_read2_b32 v[44:45], v244 offset0:16 offset1:17
	ds_read2_b32 v[46:47], v244 offset0:18 offset1:19
	ds_read2_b32 v[48:49], v244 offset0:24 offset1:25
	ds_read2_b32 v[50:51], v244 offset0:26 offset1:27
	ds_read_b128 v[240:243], v246 offset:32
	s_branch .LBB0_380
; #define LAS __attribute__((address_space(3)))
; template <bool BAND, int OUTMODE>
; __device__ __forceinline__ void compute(LAS unsigned char* lds, const bf16x8 (&qr)[4], int tid, int mq0, int dil, int res, int kt_min, int bias_tab, float sink2,
;                                         bf16* ob, int opitch, float* lsep) {
;     ...
;     for (int t = t0; t < NT; ++t) {
;         f32x16 S;
;         if (BAND) {
; #pragma unroll
;             for (int i = 0; i < 16; ++i) S[i] = bl[32 * t + (i & 3) + 8 * (i >> 2)];
;         } else {
; #pragma unroll
;             for (int i = 0; i < 16; ++i) S[i] = 0.f;
;         }
; #pragma unroll
;         for (int s = 0; s < 4; ++s) { const bf16x8 kf = *(const LAS bf16x8*)(kb + t * 32 * KSTR + s * 32); S = __builtin_amdgcn_mfma_f32_32x32x16_bf16(kf, qr[s], S, 0, 0, 0); }
;         float m0 = fmaxf(fmaxf(S[0], S[1]), fmaxf(S[2], S[3])), m1 = fmaxf(fmaxf(S[4], S[5]), fmaxf(S[6], S[7])), m2 = fmaxf(fmaxf(S[8], S[9]), fmaxf(S[10], S[11])), m3 = fmaxf(fmaxf(S[12], S[13]), fmaxf(S[14], S[15]));
;         const float mt = xhalf_max(fmaxf(fmaxf(m0, m1), fmaxf(m2, m3)));
;         if (__any(mt > mref + THR)) {
;             const float mnew = fmaxf(mref, mt), f = __builtin_amdgcn_exp2f(mref - mnew);
;             mref = mnew; l *= f;
; #pragma unroll
;             for (int i = 0; i < 16; ++i) { o0[i] *= f; o1[i] *= f; }
;         }
; #pragma unroll
;         for (int i = 0; i < 16; ++i) { const float p = __builtin_amdgcn_exp2f(S[i] - mref); S[i] = p; l += p; }
; #pragma unroll
;         for (int s = 0; s < 2; ++s) {
;             v4u pw; pw.x = cvtpk(S[8 * s + 0], S[8 * s + 1]); pw.y = cvtpk(S[8 * s + 2], S[8 * s + 3]); pw.z = cvtpk(S[8 * s + 4], S[8 * s + 5]); pw.w = cvtpk(S[8 * s + 6], S[8 * s + 7]);
;             const bf16x8 pa = __builtin_bit_cast(bf16x8, pw);
;             const LAS unsigned char* vp = vb + (32 * t + 16 * s) * 64;
;             const s16x4 a0 = vtr(vp), a1 = vtr(vp + 8 * 64), b0 = vtr(vp + VPLANE), b1 = vtr(vp + VPLANE + 8 * 64);
;             const bf16x8 v0 = __builtin_shufflevector(a0, a1, 0, 1, 2, 3, 4, 5, 6, 7), v1 = __builtin_shufflevector(b0, b1, 0, 1, 2, 3, 4, 5, 6, 7);
;             o0 = __builtin_amdgcn_mfma_f32_32x32x16_bf16(v0, pa, o0, 0, 0, 0);
;             o1 = __builtin_amdgcn_mfma_f32_32x32x16_bf16(v1, pa, o1, 0, 0, 0);
;         }
;     }
.LBB0_379:
	v_pk_add_f32 v[220:221], v[36:37], v[138:139] op_sel:[0,1] op_sel_hi:[1,1] neg_lo:[0,1] neg_hi:[0,1]
	v_pk_add_f32 v[222:223], v[38:39], v[138:139] op_sel:[0,1] op_sel_hi:[1,1] neg_lo:[0,1] neg_hi:[0,1]
	v_pk_add_f32 v[224:225], v[40:41], v[138:139] op_sel:[0,1] op_sel_hi:[1,1] neg_lo:[0,1] neg_hi:[0,1]
	v_pk_add_f32 v[226:227], v[42:43], v[138:139] op_sel:[0,1] op_sel_hi:[1,1] neg_lo:[0,1] neg_hi:[0,1]
	v_pk_add_f32 v[228:229], v[44:45], v[138:139] op_sel:[0,1] op_sel_hi:[1,1] neg_lo:[0,1] neg_hi:[0,1]
	v_pk_add_f32 v[230:231], v[46:47], v[138:139] op_sel:[0,1] op_sel_hi:[1,1] neg_lo:[0,1] neg_hi:[0,1]
	v_pk_add_f32 v[232:233], v[48:49], v[138:139] op_sel:[0,1] op_sel_hi:[1,1] neg_lo:[0,1] neg_hi:[0,1]
	v_pk_add_f32 v[234:235], v[50:51], v[138:139] op_sel:[0,1] op_sel_hi:[1,1] neg_lo:[0,1] neg_hi:[0,1]
	v_add_u32_e32 v137, 0x1200, v137
	v_add_u32_e32 v138, 0x80, v138
	v_add_u32_e32 v244, 0x19800, v138
	ds_read2_b32 v[36:37], v244 offset1:1
	ds_read2_b32 v[38:39], v244 offset0:2 offset1:3
	ds_read2_b32 v[40:41], v244 offset0:8 offset1:9
	ds_read2_b32 v[42:43], v244 offset0:10 offset1:11
	v_add_u32_e32 v246, 0, v137
	ds_read_b128 v[236:239], v246
	ds_read2_b32 v[44:45], v244 offset0:16 offset1:17
	ds_read2_b32 v[46:47], v244 offset0:18 offset1:19
	ds_read2_b32 v[48:49], v244 offset0:24 offset1:25
	ds_read2_b32 v[50:51], v244 offset0:26 offset1:27
	ds_read_b128 v[240:243], v246 offset:32
	v_exp_f32_e32 v200, v220
	v_exp_f32_e32 v201, v221
	v_exp_f32_e32 v202, v222
	v_exp_f32_e32 v203, v223
	v_exp_f32_e32 v204, v224
	v_exp_f32_e32 v205, v225
	v_exp_f32_e32 v206, v226
	v_exp_f32_e32 v207, v227
	v_add_u32_e32 v182, 0, v135
	v_exp_f32_e32 v208, v228
	ds_read_b64_tr_b16 v[190:191], v182 offset:55296
	ds_read_b64_tr_b16 v[192:193], v182 offset:55808
	v_exp_f32_e32 v209, v229
	v_add_u32_e32 v245, 0x6000, v182
	v_exp_f32_e32 v210, v230
	ds_read_b64_tr_b16 v[194:195], v245 offset:55296
	ds_read_b64_tr_b16 v[196:197], v245 offset:55808
	ds_read_b64_tr_b16 v[166:167], v182 offset:56320
	ds_read_b64_tr_b16 v[168:169], v182 offset:56832
	v_exp_f32_e32 v211, v231
	v_exp_f32_e32 v212, v232
	v_cvt_pk_bf16_f32 v186, v200, v201
	v_cvt_pk_bf16_f32 v187, v202, v203
	v_cvt_pk_bf16_f32 v188, v204, v205
	v_cvt_pk_bf16_f32 v189, v206, v207
	s_waitcnt lgkmcnt(4)
	v_mfma_f32_32x32x16_bf16 v[20:35], v[190:193], v[186:189], v[20:35]
	v_exp_f32_e32 v213, v233
	ds_read_b64_tr_b16 v[190:191], v245 offset:56320
	ds_read_b64_tr_b16 v[192:193], v245 offset:56832
	s_waitcnt lgkmcnt(4)
	v_mfma_f32_32x32x16_bf16 v[4:19], v[194:197], v[186:189], v[4:19]
	v_exp_f32_e32 v214, v234
	v_exp_f32_e32 v215, v235
	v_cvt_pk_bf16_f32 v186, v208, v209
	v_cvt_pk_bf16_f32 v187, v210, v211
	v_cvt_pk_bf16_f32 v188, v212, v213
	v_cvt_pk_bf16_f32 v189, v214, v215
	s_waitcnt lgkmcnt(2)
	v_mfma_f32_32x32x16_bf16 v[20:35], v[166:169], v[186:189], v[20:35]
	s_add_i32 s6, s6, 1
	s_waitcnt lgkmcnt(0)
	v_mfma_f32_32x32x16_bf16 v[4:19], v[190:193], v[186:189], v[4:19]
	v_pk_add_f32 v[220:221], v[200:201], v[202:203]
	v_pk_add_f32 v[222:223], v[204:205], v[206:207]
	v_pk_add_f32 v[224:225], v[208:209], v[210:211]
	v_pk_add_f32 v[226:227], v[212:213], v[214:215]
	v_pk_add_f32 v[220:221], v[220:221], v[222:223]
	v_pk_add_f32 v[224:225], v[224:225], v[226:227]
	v_pk_add_f32 v[220:221], v[220:221], v[224:225]
	v_add_f32_e32 v220, v220, v221
	v_add_f32_e32 v3, v3, v220
	v_add_u32_e32 v135, 0x800, v135
	s_cmp_lt_u32 s6, 4
	s_cbranch_scc0 .LBB0_382
.LBB0_380:
	v_add_u32_e32 v174, 0, v137
	s_waitcnt lgkmcnt(1)
	v_mfma_f32_32x32x16_bf16 v[36:51], v[236:239], v[60:63], v[36:51]
	s_waitcnt lgkmcnt(0)
	v_mfma_f32_32x32x16_bf16 v[36:51], v[240:243], v[74:77], v[36:51]
	ds_read_b128 v[166:169], v174 offset:64
	ds_read_b128 v[170:173], v174 offset:96
	s_waitcnt lgkmcnt(1)
	v_mfma_f32_32x32x16_bf16 v[36:51], v[166:169], v[78:81], v[36:51]
	s_waitcnt lgkmcnt(0)
	v_mfma_f32_32x32x16_bf16 v[36:51], v[170:173], v[82:85], v[36:51]
	s_nop 11
	v_max3_f32 v166, v36, v37, v38
	v_max3_f32 v167, v39, v40, v41
	v_max3_f32 v168, v42, v43, v44
	v_max3_f32 v169, v45, v46, v47
	v_max3_f32 v170, v48, v49, v50
	v_max3_f32 v166, v166, v167, v51
	v_max3_f32 v168, v168, v169, v170
	v_max_f32_e32 v166, v166, v168
	v_mov_b32_e32 v167, v166
	s_nop 1
	v_permlane32_swap_b32_e32 v166, v167
	v_max_f32_e32 v166, v166, v167
	v_add_f32_e32 v167, 0x41000000, v139
	v_cmp_gt_f32_e32 vcc, v166, v167
	s_cbranch_vccz .LBB0_379
	v_max_f32_e32 v166, v166, v166
	v_max_f32_e32 v167, v139, v139
	v_max_f32_e32 v167, v167, v166
	v_sub_f32_e32 v139, v139, v167
	v_exp_f32_e32 v166, v139
	v_mov_b32_e32 v139, v167
	v_pk_mul_f32 v[34:35], v[34:35], v[166:167] op_sel_hi:[1,0]
	v_pk_mul_f32 v[32:33], v[32:33], v[166:167] op_sel_hi:[1,0]
	v_pk_mul_f32 v[30:31], v[30:31], v[166:167] op_sel_hi:[1,0]
	v_pk_mul_f32 v[28:29], v[28:29], v[166:167] op_sel_hi:[1,0]
	v_pk_mul_f32 v[26:27], v[26:27], v[166:167] op_sel_hi:[1,0]
	v_pk_mul_f32 v[24:25], v[24:25], v[166:167] op_sel_hi:[1,0]
	v_pk_mul_f32 v[22:23], v[22:23], v[166:167] op_sel_hi:[1,0]
	v_pk_mul_f32 v[20:21], v[20:21], v[166:167] op_sel_hi:[1,0]
	v_pk_mul_f32 v[18:19], v[18:19], v[166:167] op_sel_hi:[1,0]
	v_pk_mul_f32 v[16:17], v[16:17], v[166:167] op_sel_hi:[1,0]
	v_pk_mul_f32 v[14:15], v[14:15], v[166:167] op_sel_hi:[1,0]
	v_pk_mul_f32 v[12:13], v[12:13], v[166:167] op_sel_hi:[1,0]
	v_pk_mul_f32 v[10:11], v[10:11], v[166:167] op_sel_hi:[1,0]
	v_pk_mul_f32 v[8:9], v[8:9], v[166:167] op_sel_hi:[1,0]
	v_pk_mul_f32 v[6:7], v[6:7], v[166:167] op_sel_hi:[1,0]
	v_pk_mul_f32 v[4:5], v[4:5], v[166:167] op_sel_hi:[1,0]
	v_mul_f32_e32 v3, v3, v166
	s_branch .LBB0_379

; #define GAS __attribute__((address_space(1)))
; #define LAS __attribute__((address_space(3)))
; __device__ __forceinline__ void issue_loads(const UnitP& P, StageRegs& R, int tid) {
;     ...
;     const long qtok = (long)(P.mq0 + 32 * wave + r32) * P.dil + P.res;
; #pragma unroll
;     for (int s = 0; s < 4; ++s) R.q[s] = *(const GAS bf16x8*)(P.qg + qtok * P.qpitch + hi * 8 + 16 * s);
; template <bool BAND, int OUTMODE>
; __device__ __forceinline__ void compute(LAS unsigned char* lds, const bf16x8 (&qr)[4], int tid, int mq0, int dil, int res, int kt_min, int bias_tab, float sink2,
;                                         bf16* ob, int opitch, float* lsep) {
;     const int lane = tid & 63, wave = __builtin_amdgcn_readfirstlane(tid >> 6), r32 = lane & 31, hi = lane >> 5;
;     constexpr int NT = BAND ? 5 : 8;
;     const int kt0 = BAND ? wave : 0;
;     int t0 = BAND ? kt_min - kt0 : 0; t0 = t0 < 0 ? 0 : t0;
;     const LAS unsigned char* kb = lds + K_OFF + (32 * kt0 + r32) * KSTR + hi * 16;
;     const LAS float* bl = (const LAS float*)(lds + B_OFF) + bias_tab * BT_FLOATS + (31 - r32 + 4 * hi);
;     const int i16 = lane & 15, q4 = i16 >> 2, p4 = i16 & 3, blk16 = (lane >> 4) & 1;
;     const LAS unsigned char* vb = lds + V_OFF + (32 * kt0 + 4 * hi + q4) * 64 + blk16 * 32 + p4 * 8;
;     float mref = -1e20f, l = 0.f;
;     f32x16 o0, o1;
; #pragma unroll
;     for (int i = 0; i < 16; ++i) { o0[i] = 0.f; o1[i] = 0.f; }
.LBB0_386:
	s_or_b64 exec, exec, s[16:17]
	s_add_i32 s0, s78, s77
	s_add_i32 s0, s0, 0xc000
	s_add_u32 s1, s34, s6
	s_addc_u32 s3, s35, 0
	s_add_u32 s12, s1, 0xee00900
	s_addc_u32 s13, s3, 0
	s_and_b32 s3, s0, 0xffffff00
	s_add_i32 s3, s3, 0xffff4000
	v_or_b32_e32 v3, s3, v152
	s_movk_i32 s0, 0xc00
	v_mov_b64_e32 v[4:5], s[12:13]
	v_mad_i64_i32 v[4:5], s[12:13], v3, s0, v[4:5]
	s_lshr_b32 s0, s5, 1
	s_add_i32 s0, s0, s42
	s_mul_i32 s0, s0, 12
	s_sub_i32 s12, s4, s0
	s_add_i32 s30, s30, 13
	s_cmp_lt_u32 s30, 23
	v_mov_b32_e32 v3, 0
	s_cselect_b32 s0, 4, 0
	s_ashr_i32 s13, s12, 31
	v_lshl_add_u64 v[4:5], v[4:5], 0, v[2:3]
	s_lshl_b64 s[4:5], s[12:13], 2
	global_load_dwordx4 v[74:77], v[4:5], off
	global_load_dwordx4 v[78:81], v[4:5], off offset:32
	global_load_dwordx4 v[82:85], v[4:5], off offset:64
	global_load_dwordx4 v[102:105], v[4:5], off offset:96
	s_add_u32 s4, s36, s4
	s_addc_u32 s5, s37, s5
	global_load_dword v130, v3, s[4:5]
	v_readfirstlane_b32 s1, v0
	s_lshr_b32 s1, s1, 6
	s_lshl_b32 s4, s1, 5
	s_sub_i32 s0, s0, s1
	v_or_b32_e32 v2, s4, v156
	s_max_i32 s0, s0, 0
	v_add_lshl_u32 v2, v2, v157, 6
	s_mul_i32 s7, s12, 0x300
	s_add_i32 s5, s0, -1
	v_lshl_add_u32 v2, s0, 11, v2
	s_mul_i32 s13, s0, 0x1200
	s_lshl_b32 s0, s0, 7
	v_or_b32_e32 v2, v2, v146
	s_add_i32 s7, s7, s0
	v_add_u32_e32 v131, v2, v147
	s_mulk_i32 s1, 0x1200
	v_or_b32_e32 v2, s7, v134
	v_mov_b32_e32 v16, v3
	v_mov_b32_e32 v17, v3
	s_add_i32 s13, s13, s1
	v_add_u32_e32 v133, v2, v165
	v_mov_b32_e32 v2, v3
	v_mov_b32_e32 v4, v3
	v_mov_b32_e32 v5, v3
	v_mov_b32_e32 v6, v3
	v_mov_b32_e32 v7, v3
	v_mov_b32_e32 v8, v3
	v_mov_b32_e32 v9, v3
	v_mov_b32_e32 v10, v3
	v_mov_b32_e32 v11, v3
	v_mov_b32_e32 v12, v3
	v_mov_b32_e32 v13, v3
	v_mov_b32_e32 v14, v3
	v_mov_b32_e32 v15, v3
	v_mov_b64_e32 v[32:33], v[16:17]
	v_mov_b64_e32 v[48:49], v[16:17]
	v_add3_u32 v132, s13, v160, v134
	v_mov_b32_e32 v135, 0xe0ad78ec
	v_mov_b64_e32 v[30:31], v[14:15]
	v_mov_b64_e32 v[28:29], v[12:13]
	v_mov_b64_e32 v[26:27], v[10:11]
	v_mov_b64_e32 v[24:25], v[8:9]
	v_mov_b64_e32 v[22:23], v[6:7]
	v_mov_b64_e32 v[20:21], v[4:5]
	v_mov_b64_e32 v[18:19], v[2:3]
	v_mov_b64_e32 v[46:47], v[14:15]
	v_mov_b64_e32 v[44:45], v[12:13]
	v_mov_b64_e32 v[42:43], v[10:11]
	v_mov_b64_e32 v[40:41], v[8:9]
	v_mov_b64_e32 v[38:39], v[6:7]
	v_mov_b64_e32 v[36:37], v[4:5]
	v_mov_b64_e32 v[34:35], v[2:3]
	v_add_u32_e32 v244, 0x19800, v133
	ds_read2_b32 v[50:51], v244 offset1:1
	ds_read2_b32 v[52:53], v244 offset0:2 offset1:3
	ds_read2_b32 v[54:55], v244 offset0:8 offset1:9
	ds_read2_b32 v[56:57], v244 offset0:10 offset1:11
	v_add_u32_e32 v246, 0, v132
	ds_read_b128 v[236:239], v246
	ds_read2_b32 v[58:59], v244 offset0:16 offset1:17
	ds_read2_b32 v[60:61], v244 offset0:18 offset1:19
	ds_read2_b32 v[62:63], v244 offset0:24 offset1:25
	ds_read2_b32 v[64:65], v244 offset0:26 offset1:27
	ds_read_b128 v[240:243], v246 offset:32
	s_branch .LBB0_388
; #define LAS __attribute__((address_space(3)))
; template <bool BAND, int OUTMODE>
; __device__ __forceinline__ void compute(LAS unsigned char* lds, const bf16x8 (&qr)[4], int tid, int mq0, int dil, int res, int kt_min, int bias_tab, float sink2,
;                                         bf16* ob, int opitch, float* lsep) {
;     ...
;     for (int t = t0; t < NT; ++t) {
;         f32x16 S;
;         if (BAND) {
; #pragma unroll
;             for (int i = 0; i < 16; ++i) S[i] = bl[32 * t + (i & 3) + 8 * (i >> 2)];
;         } else {
; #pragma unroll
;             for (int i = 0; i < 16; ++i) S[i] = 0.f;
;         }
; #pragma unroll
;         for (int s = 0; s < 4; ++s) { const bf16x8 kf = *(const LAS bf16x8*)(kb + t * 32 * KSTR + s * 32); S = __builtin_amdgcn_mfma_f32_32x32x16_bf16(kf, qr[s], S, 0, 0, 0); }
;         float m0 = fmaxf(fmaxf(S[0], S[1]), fmaxf(S[2], S[3])), m1 = fmaxf(fmaxf(S[4], S[5]), fmaxf(S[6], S[7])), m2 = fmaxf(fmaxf(S[8], S[9]), fmaxf(S[10], S[11])), m3 = fmaxf(fmaxf(S[12], S[13]), fmaxf(S[14], S[15]));
;         const float mt = xhalf_max(fmaxf(fmaxf(m0, m1), fmaxf(m2, m3)));
;         if (__any(mt > mref + THR)) {
;             const float mnew = fmaxf(mref, mt), f = __builtin_amdgcn_exp2f(mref - mnew);
;             mref = mnew; l *= f;
; #pragma unroll
;             for (int i = 0; i < 16; ++i) { o0[i] *= f; o1[i] *= f; }
;         }
; #pragma unroll
;         for (int i = 0; i < 16; ++i) { const float p = __builtin_amdgcn_exp2f(S[i] - mref); S[i] = p; l += p; }
; #pragma unroll
;         for (int s = 0; s < 2; ++s) {
;             v4u pw; pw.x = cvtpk(S[8 * s + 0], S[8 * s + 1]); pw.y = cvtpk(S[8 * s + 2], S[8 * s + 3]); pw.z = cvtpk(S[8 * s + 4], S[8 * s + 5]); pw.w = cvtpk(S[8 * s + 6], S[8 * s + 7]);
;             const bf16x8 pa = __builtin_bit_cast(bf16x8, pw);
;             const LAS unsigned char* vp = vb + (32 * t + 16 * s) * 64;
;             const s16x4 a0 = vtr(vp), a1 = vtr(vp + 8 * 64), b0 = vtr(vp + VPLANE), b1 = vtr(vp + VPLANE + 8 * 64);
;             const bf16x8 v0 = __builtin_shufflevector(a0, a1, 0, 1, 2, 3, 4, 5, 6, 7), v1 = __builtin_shufflevector(b0, b1, 0, 1, 2, 3, 4, 5, 6, 7);
;             o0 = __builtin_amdgcn_mfma_f32_32x32x16_bf16(v0, pa, o0, 0, 0, 0);
;             o1 = __builtin_amdgcn_mfma_f32_32x32x16_bf16(v1, pa, o1, 0, 0, 0);
;         }
;     }
.LBB0_387:
	v_pk_add_f32 v[220:221], v[50:51], v[134:135] op_sel:[0,1] op_sel_hi:[1,1] neg_lo:[0,1] neg_hi:[0,1]
	v_pk_add_f32 v[222:223], v[52:53], v[134:135] op_sel:[0,1] op_sel_hi:[1,1] neg_lo:[0,1] neg_hi:[0,1]
	v_pk_add_f32 v[224:225], v[54:55], v[134:135] op_sel:[0,1] op_sel_hi:[1,1] neg_lo:[0,1] neg_hi:[0,1]
	v_pk_add_f32 v[226:227], v[56:57], v[134:135] op_sel:[0,1] op_sel_hi:[1,1] neg_lo:[0,1] neg_hi:[0,1]
	v_pk_add_f32 v[228:229], v[58:59], v[134:135] op_sel:[0,1] op_sel_hi:[1,1] neg_lo:[0,1] neg_hi:[0,1]
	v_pk_add_f32 v[230:231], v[60:61], v[134:135] op_sel:[0,1] op_sel_hi:[1,1] neg_lo:[0,1] neg_hi:[0,1]
	v_pk_add_f32 v[232:233], v[62:63], v[134:135] op_sel:[0,1] op_sel_hi:[1,1] neg_lo:[0,1] neg_hi:[0,1]
	v_pk_add_f32 v[234:235], v[64:65], v[134:135] op_sel:[0,1] op_sel_hi:[1,1] neg_lo:[0,1] neg_hi:[0,1]
	v_add_u32_e32 v132, 0x1200, v132
	v_add_u32_e32 v133, 0x80, v133
	v_add_u32_e32 v244, 0x19800, v133
	ds_read2_b32 v[50:51], v244 offset1:1
	ds_read2_b32 v[52:53], v244 offset0:2 offset1:3
	ds_read2_b32 v[54:55], v244 offset0:8 offset1:9
	ds_read2_b32 v[56:57], v244 offset0:10 offset1:11
	v_add_u32_e32 v246, 0, v132
	ds_read_b128 v[236:239], v246
	ds_read2_b32 v[58:59], v244 offset0:16 offset1:17
	ds_read2_b32 v[60:61], v244 offset0:18 offset1:19
	ds_read2_b32 v[62:63], v244 offset0:24 offset1:25
	ds_read2_b32 v[64:65], v244 offset0:26 offset1:27
	ds_read_b128 v[240:243], v246 offset:32
	v_exp_f32_e32 v201, v221
	v_exp_f32_e32 v202, v222
	v_exp_f32_e32 v203, v223
	v_exp_f32_e32 v204, v224
	v_exp_f32_e32 v205, v225
	v_exp_f32_e32 v206, v226
	v_exp_f32_e32 v207, v227
	v_add_u32_e32 v137, 0, v131
	v_exp_f32_e32 v200, v220
	v_exp_f32_e32 v208, v228
	ds_read_b64_tr_b16 v[8:9], v137 offset:55296
	ds_read_b64_tr_b16 v[10:11], v137 offset:55808
	v_exp_f32_e32 v209, v229
	v_add_u32_e32 v245, 0x6000, v137
	v_exp_f32_e32 v210, v230
	ds_read_b64_tr_b16 v[12:13], v245 offset:55296
	ds_read_b64_tr_b16 v[14:15], v245 offset:55808
	ds_read_b64_tr_b16 v[186:187], v137 offset:56320
	ds_read_b64_tr_b16 v[188:189], v137 offset:56832
	v_exp_f32_e32 v211, v231
	v_exp_f32_e32 v212, v232
	v_cvt_pk_bf16_f32 v4, v200, v201
	v_cvt_pk_bf16_f32 v5, v202, v203
	v_cvt_pk_bf16_f32 v6, v204, v205
	v_cvt_pk_bf16_f32 v7, v206, v207
	s_waitcnt lgkmcnt(4)
	v_mfma_f32_32x32x16_bf16 v[34:49], v[8:11], v[4:7], v[34:49]
	v_exp_f32_e32 v213, v233
	ds_read_b64_tr_b16 v[8:9], v245 offset:56320
	ds_read_b64_tr_b16 v[10:11], v245 offset:56832
	s_waitcnt lgkmcnt(4)
	v_mfma_f32_32x32x16_bf16 v[18:33], v[12:15], v[4:7], v[18:33]
	v_exp_f32_e32 v214, v234
	v_exp_f32_e32 v215, v235
	v_cvt_pk_bf16_f32 v4, v208, v209
	v_cvt_pk_bf16_f32 v5, v210, v211
	v_cvt_pk_bf16_f32 v6, v212, v213
	v_cvt_pk_bf16_f32 v7, v214, v215
	s_waitcnt lgkmcnt(2)
	v_mfma_f32_32x32x16_bf16 v[34:49], v[186:189], v[4:7], v[34:49]
	s_add_i32 s5, s5, 1
	s_waitcnt lgkmcnt(0)
	v_mfma_f32_32x32x16_bf16 v[18:33], v[8:11], v[4:7], v[18:33]
	v_pk_add_f32 v[220:221], v[200:201], v[202:203]
	v_pk_add_f32 v[222:223], v[204:205], v[206:207]
	v_pk_add_f32 v[224:225], v[208:209], v[210:211]
	v_pk_add_f32 v[226:227], v[212:213], v[214:215]
	v_pk_add_f32 v[220:221], v[220:221], v[222:223]
	v_pk_add_f32 v[224:225], v[224:225], v[226:227]
	v_pk_add_f32 v[220:221], v[220:221], v[224:225]
	v_add_f32_e32 v220, v220, v221
	v_add_f32_e32 v3, v3, v220
	v_add_u32_e32 v131, 0x800, v131
	s_cmp_lt_u32 s5, 4
	s_cbranch_scc0 .LBB0_390
.LBB0_388:
	v_add_u32_e32 v12, 0, v132
	s_waitcnt lgkmcnt(1)
	v_mfma_f32_32x32x16_bf16 v[50:65], v[236:239], v[86:89], v[50:65]
	s_waitcnt lgkmcnt(0)
	v_mfma_f32_32x32x16_bf16 v[50:65], v[240:243], v[90:93], v[50:65]
	ds_read_b128 v[4:7], v12 offset:64
	ds_read_b128 v[8:11], v12 offset:96
	s_waitcnt lgkmcnt(1)
	v_mfma_f32_32x32x16_bf16 v[50:65], v[4:7], v[94:97], v[50:65]
	s_waitcnt lgkmcnt(0)
	v_mfma_f32_32x32x16_bf16 v[50:65], v[8:11], v[98:101], v[50:65]
	s_nop 11
	v_max3_f32 v2, v50, v51, v52
	v_max3_f32 v4, v53, v54, v55
	v_max3_f32 v5, v56, v57, v58
	v_max3_f32 v6, v59, v60, v61
	v_max3_f32 v7, v62, v63, v64
	v_max3_f32 v2, v2, v4, v65
	v_max3_f32 v5, v5, v6, v7
	v_max_f32_e32 v2, v2, v5
	v_mov_b32_e32 v4, v2
	s_nop 1
	v_permlane32_swap_b32_e32 v2, v4
	v_max_f32_e32 v2, v2, v4
	v_add_f32_e32 v4, 0x41000000, v135
	v_cmp_gt_f32_e32 vcc, v2, v4
	s_cbranch_vccz .LBB0_387
	v_max_f32_e32 v2, v2, v2
	v_max_f32_e32 v4, v135, v135
	v_max_f32_e32 v4, v4, v2
	v_sub_f32_e32 v2, v135, v4
	v_exp_f32_e32 v2, v2
	v_mov_b32_e32 v135, v4
	v_pk_mul_f32 v[48:49], v[48:49], v[2:3] op_sel_hi:[1,0]
	v_pk_mul_f32 v[46:47], v[46:47], v[2:3] op_sel_hi:[1,0]
	v_pk_mul_f32 v[44:45], v[44:45], v[2:3] op_sel_hi:[1,0]
	v_pk_mul_f32 v[42:43], v[42:43], v[2:3] op_sel_hi:[1,0]
	v_pk_mul_f32 v[40:41], v[40:41], v[2:3] op_sel_hi:[1,0]
	v_pk_mul_f32 v[38:39], v[38:39], v[2:3] op_sel_hi:[1,0]
	v_pk_mul_f32 v[36:37], v[36:37], v[2:3] op_sel_hi:[1,0]
	v_pk_mul_f32 v[34:35], v[34:35], v[2:3] op_sel_hi:[1,0]
	v_pk_mul_f32 v[32:33], v[32:33], v[2:3] op_sel_hi:[1,0]
	v_pk_mul_f32 v[30:31], v[30:31], v[2:3] op_sel_hi:[1,0]
	v_pk_mul_f32 v[28:29], v[28:29], v[2:3] op_sel_hi:[1,0]
	v_pk_mul_f32 v[26:27], v[26:27], v[2:3] op_sel_hi:[1,0]
	v_pk_mul_f32 v[24:25], v[24:25], v[2:3] op_sel_hi:[1,0]
	v_pk_mul_f32 v[22:23], v[22:23], v[2:3] op_sel_hi:[1,0]
	v_pk_mul_f32 v[20:21], v[20:21], v[2:3] op_sel_hi:[1,0]
	v_pk_mul_f32 v[18:19], v[18:19], v[2:3] op_sel_hi:[1,0]
	v_mul_f32_e32 v3, v3, v2
	s_branch .LBB0_387

; template <bool BAND, int OUTMODE>
; __device__ __forceinline__ void compute(LAS unsigned char* lds, const bf16x8 (&qr)[4], int tid, int mq0, int dil, int res, int kt_min, int bias_tab, float sink2,
;                                         bf16* ob, int opitch, float* lsep) {
;     ...
;     const LAS unsigned char* kb = lds + K_OFF + (32 * kt0 + r32) * KSTR + hi * 16;
;     const LAS float* bl = (const LAS float*)(lds + B_OFF) + bias_tab * BT_FLOATS + (31 - r32 + 4 * hi);
;     const int i16 = lane & 15, q4 = i16 >> 2, p4 = i16 & 3, blk16 = (lane >> 4) & 1;
;     const LAS unsigned char* vb = lds + V_OFF + (32 * kt0 + 4 * hi + q4) * 64 + blk16 * 32 + p4 * 8;
;     float mref = -1e20f, l = 0.f;
;     f32x16 o0, o1;
; #pragma unroll
;     for (int i = 0; i < 16; ++i) { o0[i] = 0.f; o1[i] = 0.f; }
; #pragma unroll 1
;     for (int t = t0; t < NT; ++t) {
;         f32x16 S;
;         if (BAND) {
; #pragma unroll
;             for (int i = 0; i < 16; ++i) S[i] = bl[32 * t + (i & 3) + 8 * (i >> 2)];
;         } else {
; #pragma unroll
;             for (int i = 0; i < 16; ++i) S[i] = 0.f;
;         }
; #pragma unroll
;         for (int s = 0; s < 4; ++s) { const bf16x8 kf = *(const LAS bf16x8*)(kb + t * 32 * KSTR + s * 32); S = __builtin_amdgcn_mfma_f32_32x32x16_bf16(kf, qr[s], S, 0, 0, 0); }
;         float m0 = fmaxf(fmaxf(S[0], S[1]), fmaxf(S[2], S[3])), m1 = fmaxf(fmaxf(S[4], S[5]), fmaxf(S[6], S[7])), m2 = fmaxf(fmaxf(S[8], S[9]), fmaxf(S[10], S[11])), m3 = fmaxf(fmaxf(S[12], S[13]), fmaxf(S[14], S[15]));
;         const float mt = xhalf_max(fmaxf(fmaxf(m0, m1), fmaxf(m2, m3)));
;         if (__any(mt > mref + THR)) {
;             const float mnew = fmaxf(mref, mt), f = __builtin_amdgcn_exp2f(mref - mnew);
;             mref = mnew; l *= f;
; #pragma unroll
;             for (int i = 0; i < 16; ++i) { o0[i] *= f; o1[i] *= f; }
;         }
; #pragma unroll
;         for (int i = 0; i < 16; ++i) { const float p = __builtin_amdgcn_exp2f(S[i] - mref); S[i] = p; l += p; }
; #pragma unroll
;         for (int s = 0; s < 2; ++s) {
;             v4u pw; pw.x = cvtpk(S[8 * s + 0], S[8 * s + 1]); pw.y = cvtpk(S[8 * s + 2], S[8 * s + 3]); pw.z = cvtpk(S[8 * s + 4], S[8 * s + 5]); pw.w = cvtpk(S[8 * s + 6], S[8 * s + 7]);
;             const bf16x8 pa = __builtin_bit_cast(bf16x8, pw);
;             const LAS unsigned char* vp = vb + (32 * t + 16 * s) * 64;
.LBB0_392:
	s_or_b64 exec, exec, s[12:13]
	v_mul_u32_u24_e32 v2, 0xf0, v145
	v_and_b32_e32 v3, 0xc0, v140
	s_waitcnt lgkmcnt(0)
	s_barrier
	v_add3_u32 v2, v2, v3, v146
	v_mov_b32_e32 v16, v139
	v_mov_b32_e32 v17, v139
	s_movk_i32 s0, 0x90
	v_add3_u32 v51, v2, v147, 0
	v_mov_b32_e32 v2, v139
	v_mov_b32_e32 v3, v139
	v_mov_b32_e32 v4, v139
	v_mov_b32_e32 v5, v139
	v_mov_b32_e32 v6, v139
	v_mov_b32_e32 v7, v139
	v_mov_b32_e32 v8, v139
	v_mov_b32_e32 v9, v139
	v_mov_b32_e32 v10, v139
	v_mov_b32_e32 v11, v139
	v_mov_b32_e32 v12, v139
	v_mov_b32_e32 v13, v139
	v_mov_b32_e32 v14, v139
	v_mov_b32_e32 v15, v139
	v_mov_b64_e32 v[32:33], v[16:17]
	v_mad_u32_u24 v50, v164, s0, 0
	v_mov_b32_e32 v52, 0xe0ad78ec
	s_mov_b32 s4, 8
	v_mov_b64_e32 v[30:31], v[14:15]
	v_mov_b64_e32 v[28:29], v[12:13]
	v_mov_b64_e32 v[26:27], v[10:11]
	v_mov_b64_e32 v[24:25], v[8:9]
	v_mov_b64_e32 v[22:23], v[6:7]
	v_mov_b64_e32 v[20:21], v[4:5]
	v_mov_b64_e32 v[18:19], v[2:3]
	v_add_u32_e32 v246, v50, v134
	ds_read_b128 v[236:239], v246
	ds_read_b128 v[240:243], v246 offset:32
	s_branch .LBB0_394
.LBB0_393:
	v_pk_add_f32 v[220:221], v[34:35], v[52:53] op_sel_hi:[1,0] neg_lo:[0,1] neg_hi:[0,1]
	v_pk_add_f32 v[222:223], v[36:37], v[52:53] op_sel_hi:[1,0] neg_lo:[0,1] neg_hi:[0,1]
	v_pk_add_f32 v[224:225], v[38:39], v[52:53] op_sel_hi:[1,0] neg_lo:[0,1] neg_hi:[0,1]
	v_pk_add_f32 v[226:227], v[40:41], v[52:53] op_sel_hi:[1,0] neg_lo:[0,1] neg_hi:[0,1]
	v_pk_add_f32 v[228:229], v[42:43], v[52:53] op_sel_hi:[1,0] neg_lo:[0,1] neg_hi:[0,1]
	v_pk_add_f32 v[230:231], v[44:45], v[52:53] op_sel_hi:[1,0] neg_lo:[0,1] neg_hi:[0,1]
	v_pk_add_f32 v[232:233], v[46:47], v[52:53] op_sel_hi:[1,0] neg_lo:[0,1] neg_hi:[0,1]
	v_pk_add_f32 v[234:235], v[48:49], v[52:53] op_sel_hi:[1,0] neg_lo:[0,1] neg_hi:[0,1]
	v_add_u32_e32 v50, 0x1200, v50
	v_add_u32_e32 v246, v50, v134
	ds_read_b128 v[236:239], v246
	ds_read_b128 v[240:243], v246 offset:32
	v_exp_f32_e32 v200, v220
	v_exp_f32_e32 v201, v221
	v_exp_f32_e32 v202, v222
	v_exp_f32_e32 v203, v223
	v_exp_f32_e32 v204, v224
	v_exp_f32_e32 v205, v225
	v_exp_f32_e32 v206, v226
	v_exp_f32_e32 v207, v227
	v_add_u32_e32 v69, v51, v134
	v_exp_f32_e32 v208, v228
	ds_read_b64_tr_b16 v[38:39], v69 offset:55296
	ds_read_b64_tr_b16 v[40:41], v69 offset:55808
	v_exp_f32_e32 v209, v229
	v_add_u32_e32 v245, 0x6000, v69
	v_exp_f32_e32 v210, v230
	ds_read_b64_tr_b16 v[42:43], v245 offset:55296
	ds_read_b64_tr_b16 v[44:45], v245 offset:55808
	ds_read_b64_tr_b16 v[54:55], v69 offset:56320
	ds_read_b64_tr_b16 v[56:57], v69 offset:56832
	v_exp_f32_e32 v211, v231
	v_exp_f32_e32 v212, v232
	v_cvt_pk_bf16_f32 v34, v200, v201
	v_cvt_pk_bf16_f32 v35, v202, v203
	v_cvt_pk_bf16_f32 v36, v204, v205
	v_cvt_pk_bf16_f32 v37, v206, v207
	s_add_i32 s4, s4, -1
	s_waitcnt lgkmcnt(4)
	v_mfma_f32_32x32x16_bf16 v[18:33], v[38:41], v[34:37], v[18:33]
	v_exp_f32_e32 v213, v233
	ds_read_b64_tr_b16 v[38:39], v245 offset:56320
	ds_read_b64_tr_b16 v[40:41], v245 offset:56832
	v_add_u32_e32 v51, 0x800, v51
	s_cmp_lg_u32 s4, 0
	s_waitcnt lgkmcnt(4)
	v_mfma_f32_32x32x16_bf16 v[2:17], v[42:45], v[34:37], v[2:17]
	v_exp_f32_e32 v214, v234
	v_exp_f32_e32 v215, v235
	v_cvt_pk_bf16_f32 v34, v208, v209
	v_cvt_pk_bf16_f32 v35, v210, v211
	v_cvt_pk_bf16_f32 v36, v212, v213
	v_cvt_pk_bf16_f32 v37, v214, v215
	s_waitcnt lgkmcnt(2)
	v_mfma_f32_32x32x16_bf16 v[18:33], v[54:57], v[34:37], v[18:33]
	s_waitcnt lgkmcnt(0)
	v_mfma_f32_32x32x16_bf16 v[2:17], v[38:41], v[34:37], v[2:17]
	v_pk_add_f32 v[220:221], v[200:201], v[202:203]
	v_pk_add_f32 v[222:223], v[204:205], v[206:207]
	v_pk_add_f32 v[224:225], v[208:209], v[210:211]
	v_pk_add_f32 v[226:227], v[212:213], v[214:215]
	v_pk_add_f32 v[220:221], v[220:221], v[222:223]
	v_pk_add_f32 v[224:225], v[224:225], v[226:227]
	v_pk_add_f32 v[220:221], v[220:221], v[224:225]
	v_add_f32_e32 v220, v220, v221
	v_add_f32_e32 v139, v139, v220
	s_cbranch_scc0 .LBB0_396
.LBB0_394:
	v_add_u32_e32 v53, v50, v134
	s_waitcnt lgkmcnt(1)
	v_mfma_f32_32x32x16_bf16 v[34:49], v[236:239], v[74:77], 0
	s_waitcnt lgkmcnt(0)
	v_mfma_f32_32x32x16_bf16 v[34:49], v[240:243], v[78:81], v[34:49]
	ds_read_b128 v[54:57], v53 offset:64
	ds_read_b128 v[58:61], v53 offset:96
	s_waitcnt lgkmcnt(1)
	v_mfma_f32_32x32x16_bf16 v[34:49], v[54:57], v[82:85], v[34:49]
	s_waitcnt lgkmcnt(0)
	v_mfma_f32_32x32x16_bf16 v[34:49], v[58:61], v[102:105], v[34:49]
	s_nop 11
	v_max3_f32 v53, v34, v35, v36
	v_max3_f32 v54, v37, v38, v39
	v_max3_f32 v55, v40, v41, v42
	v_max3_f32 v56, v43, v44, v45
	v_max3_f32 v57, v46, v47, v48
	v_max3_f32 v53, v53, v54, v49
	v_max3_f32 v55, v55, v56, v57
	v_max_f32_e32 v53, v53, v55
	v_mov_b32_e32 v54, v53
	s_nop 1
	v_permlane32_swap_b32_e32 v53, v54
	v_max_f32_e32 v53, v53, v54
	v_add_f32_e32 v54, 0x41000000, v52
	v_cmp_gt_f32_e32 vcc, v53, v54
	s_cbranch_vccz .LBB0_393
	v_max_f32_e32 v53, v53, v53
	v_max_f32_e32 v54, v52, v52
	v_max_f32_e32 v53, v54, v53
	v_sub_f32_e32 v52, v52, v53
	v_exp_f32_e32 v52, v52
	s_nop 0
	v_pk_mul_f32 v[32:33], v[32:33], v[52:53] op_sel_hi:[1,0]
	v_pk_mul_f32 v[30:31], v[30:31], v[52:53] op_sel_hi:[1,0]
	v_pk_mul_f32 v[28:29], v[28:29], v[52:53] op_sel_hi:[1,0]
	v_pk_mul_f32 v[26:27], v[26:27], v[52:53] op_sel_hi:[1,0]
	v_pk_mul_f32 v[24:25], v[24:25], v[52:53] op_sel_hi:[1,0]
	v_pk_mul_f32 v[22:23], v[22:23], v[52:53] op_sel_hi:[1,0]
	v_pk_mul_f32 v[20:21], v[20:21], v[52:53] op_sel_hi:[1,0]
	v_pk_mul_f32 v[18:19], v[18:19], v[52:53] op_sel_hi:[1,0]
	v_pk_mul_f32 v[16:17], v[16:17], v[52:53] op_sel_hi:[1,0]
	v_pk_mul_f32 v[14:15], v[14:15], v[52:53] op_sel_hi:[1,0]
	v_pk_mul_f32 v[12:13], v[12:13], v[52:53] op_sel_hi:[1,0]
	v_pk_mul_f32 v[10:11], v[10:11], v[52:53] op_sel_hi:[1,0]
	v_pk_mul_f32 v[8:9], v[8:9], v[52:53] op_sel_hi:[1,0]
	v_pk_mul_f32 v[6:7], v[6:7], v[52:53] op_sel_hi:[1,0]
	v_pk_mul_f32 v[4:5], v[4:5], v[52:53] op_sel_hi:[1,0]
	v_pk_mul_f32 v[2:3], v[2:3], v[52:53] op_sel_hi:[1,0]
	v_mul_f32_e32 v139, v139, v52
	v_mov_b32_e32 v52, v53
	s_branch .LBB0_393

; #define GAS __attribute__((address_space(1)))
; #define LAS __attribute__((address_space(3)))
; __device__ __forceinline__ void issue_loads(const UnitP& P, StageRegs& R, int tid) {
;     ...
;     const long qtok = (long)(P.mq0 + 32 * wave + r32) * P.dil + P.res;
; #pragma unroll
;     for (int s = 0; s < 4; ++s) R.q[s] = *(const GAS bf16x8*)(P.qg + qtok * P.qpitch + hi * 8 + 16 * s);
; template <bool BAND, int OUTMODE>
; __device__ __forceinline__ void compute(LAS unsigned char* lds, const bf16x8 (&qr)[4], int tid, int mq0, int dil, int res, int kt_min, int bias_tab, float sink2,
;                                         bf16* ob, int opitch, float* lsep) {
;     const int lane = tid & 63, wave = __builtin_amdgcn_readfirstlane(tid >> 6), r32 = lane & 31, hi = lane >> 5;
;     constexpr int NT = BAND ? 5 : 8;
;     const int kt0 = BAND ? wave : 0;
;     int t0 = BAND ? kt_min - kt0 : 0; t0 = t0 < 0 ? 0 : t0;
;     const LAS unsigned char* kb = lds + K_OFF + (32 * kt0 + r32) * KSTR + hi * 16;
;     const LAS float* bl = (const LAS float*)(lds + B_OFF) + bias_tab * BT_FLOATS + (31 - r32 + 4 * hi);
;     const int i16 = lane & 15, q4 = i16 >> 2, p4 = i16 & 3, blk16 = (lane >> 4) & 1;
;     const LAS unsigned char* vb = lds + V_OFF + (32 * kt0 + 4 * hi + q4) * 64 + blk16 * 32 + p4 * 8;
;     float mref = -1e20f, l = 0.f;
;     f32x16 o0, o1;
; #pragma unroll
;     for (int i = 0; i < 16; ++i) { o0[i] = 0.f; o1[i] = 0.f; }
.LBB0_939:
	s_or_b64 exec, exec, s[16:17]
	s_add_u32 s0, s34, s24
	s_addc_u32 s1, s35, 0
	v_add_u32_e32 v4, s31, v141
	s_add_u32 s6, s0, 0x9a00600
	v_ashrrev_i32_e32 v5, 31, v4
	s_addc_u32 s7, s1, 0
	v_lshlrev_b64 v[4:5], 2, v[4:5]
	v_or_b32_e32 v4, s30, v4
	v_mov_b64_e32 v[6:7], s[6:7]
	v_mad_u64_u32 v[6:7], s[6:7], v4, s5, v[6:7]
	v_mad_i32_i24 v7, v5, s5, v7
	v_mov_b32_e32 v137, v3
	v_lshl_add_u64 v[4:5], v[6:7], 0, v[136:137]
	global_load_dwordx4 v[60:63], v[4:5], off
	global_load_dwordx4 v[74:77], v[4:5], off offset:32
	global_load_dwordx4 v[78:81], v[4:5], off offset:64
	global_load_dwordx4 v[82:85], v[4:5], off offset:96
	s_cmp_lt_u32 s2, 4
	v_readfirstlane_b32 s1, v0
	v_bfe_u32 v146, v0, 5, 1
	s_cselect_b32 s0, 4, 0
	s_lshr_b32 s1, s1, 6
	v_lshlrev_b32_e32 v157, 2, v146
	v_and_b32_e32 v158, 3, v45
	v_lshlrev_b32_e32 v5, 1, v0
	s_lshl_b32 s5, s1, 5
	s_waitcnt lgkmcnt(11)
	v_and_b32_e32 v147, 32, v5
	s_sub_i32 s0, s0, s1
	v_or3_b32 v5, s5, v157, v158
	s_max_i32 s0, s0, 0
	v_lshlrev_b32_e32 v5, 6, v5
	s_mul_i32 s25, s4, 0x300
	s_add_i32 s6, s0, -1
	v_lshl_add_u32 v5, s0, 11, v5
	s_mul_i32 s7, s0, 0x1200
	s_lshl_b32 s0, s0, 7
	v_lshlrev_b32_e32 v134, 4, v146
	v_xor_b32_e32 v4, 31, v164
	v_and_b32_e32 v148, 24, v44
	s_add_i32 s0, s25, s0
	v_or3_b32 v135, v5, v147, v148
	s_mulk_i32 s1, 0x1200
	v_or_b32_e32 v5, s0, v134
	v_lshlrev_b32_e32 v161, 2, v4
	v_mov_b32_e32 v18, v3
	v_mov_b32_e32 v19, v3
	s_add_i32 s7, s7, s1
	v_mul_u32_u24_e32 v160, 0x90, v164
	v_add_u32_e32 v167, v5, v161
	v_mov_b32_e32 v4, v3
	v_mov_b32_e32 v5, v3
	v_mov_b32_e32 v6, v3
	v_mov_b32_e32 v7, v3
	v_mov_b32_e32 v8, v3
	v_mov_b32_e32 v9, v3
	v_mov_b32_e32 v10, v3
	v_mov_b32_e32 v11, v3
	v_mov_b32_e32 v12, v3
	v_mov_b32_e32 v13, v3
	v_mov_b32_e32 v14, v3
	v_mov_b32_e32 v15, v3
	v_mov_b32_e32 v16, v3
	v_mov_b32_e32 v17, v3
	v_mov_b64_e32 v[34:35], v[18:19]
	v_mul_u32_u24_e32 v159, 0x90, v151
	v_mul_u32_u24_e32 v137, 0x90, v152
	v_mul_u32_u24_e32 v73, 0x90, v150
	v_add3_u32 v149, s7, v160, v134
	v_mov_b32_e32 v165, 0xe0ad78ec
	v_mov_b64_e32 v[32:33], v[16:17]
	v_mov_b64_e32 v[30:31], v[14:15]
	v_mov_b64_e32 v[28:29], v[12:13]
	v_mov_b64_e32 v[26:27], v[10:11]
	v_mov_b64_e32 v[24:25], v[8:9]
	v_mov_b64_e32 v[22:23], v[6:7]
	v_mov_b64_e32 v[20:21], v[4:5]
	v_add_u32_e32 v244, 0x19800, v167
	ds_read2_b32 v[36:37], v244 offset1:1
	ds_read2_b32 v[38:39], v244 offset0:2 offset1:3
	ds_read2_b32 v[40:41], v244 offset0:8 offset1:9
	ds_read2_b32 v[42:43], v244 offset0:10 offset1:11
	v_add_u32_e32 v246, 0, v149
	ds_read_b128 v[236:239], v246
	ds_read2_b32 v[44:45], v244 offset0:16 offset1:17
	ds_read2_b32 v[46:47], v244 offset0:18 offset1:19
	ds_read2_b32 v[48:49], v244 offset0:24 offset1:25
	ds_read2_b32 v[50:51], v244 offset0:26 offset1:27
	ds_read_b128 v[240:243], v246 offset:32
	s_branch .LBB0_941
; #define LAS __attribute__((address_space(3)))
; template <bool BAND, int OUTMODE>
; __device__ __forceinline__ void compute(LAS unsigned char* lds, const bf16x8 (&qr)[4], int tid, int mq0, int dil, int res, int kt_min, int bias_tab, float sink2,
;                                         bf16* ob, int opitch, float* lsep) {
;     ...
;     for (int t = t0; t < NT; ++t) {
;         f32x16 S;
;         if (BAND) {
; #pragma unroll
;             for (int i = 0; i < 16; ++i) S[i] = bl[32 * t + (i & 3) + 8 * (i >> 2)];
;         } else {
; #pragma unroll
;             for (int i = 0; i < 16; ++i) S[i] = 0.f;
;         }
; #pragma unroll
;         for (int s = 0; s < 4; ++s) { const bf16x8 kf = *(const LAS bf16x8*)(kb + t * 32 * KSTR + s * 32); S = __builtin_amdgcn_mfma_f32_32x32x16_bf16(kf, qr[s], S, 0, 0, 0); }
;         float m0 = fmaxf(fmaxf(S[0], S[1]), fmaxf(S[2], S[3])), m1 = fmaxf(fmaxf(S[4], S[5]), fmaxf(S[6], S[7])), m2 = fmaxf(fmaxf(S[8], S[9]), fmaxf(S[10], S[11])), m3 = fmaxf(fmaxf(S[12], S[13]), fmaxf(S[14], S[15]));
;         const float mt = xhalf_max(fmaxf(fmaxf(m0, m1), fmaxf(m2, m3)));
;         if (__any(mt > mref + THR)) {
;             const float mnew = fmaxf(mref, mt), f = __builtin_amdgcn_exp2f(mref - mnew);
;             mref = mnew; l *= f;
; #pragma unroll
;             for (int i = 0; i < 16; ++i) { o0[i] *= f; o1[i] *= f; }
;         }
; #pragma unroll
;         for (int i = 0; i < 16; ++i) { const float p = __builtin_amdgcn_exp2f(S[i] - mref); S[i] = p; l += p; }
; #pragma unroll
;         for (int s = 0; s < 2; ++s) {
;             v4u pw; pw.x = cvtpk(S[8 * s + 0], S[8 * s + 1]); pw.y = cvtpk(S[8 * s + 2], S[8 * s + 3]); pw.z = cvtpk(S[8 * s + 4], S[8 * s + 5]); pw.w = cvtpk(S[8 * s + 6], S[8 * s + 7]);
;             const bf16x8 pa = __builtin_bit_cast(bf16x8, pw);
;             const LAS unsigned char* vp = vb + (32 * t + 16 * s) * 64;
;             const s16x4 a0 = vtr(vp), a1 = vtr(vp + 8 * 64), b0 = vtr(vp + VPLANE), b1 = vtr(vp + VPLANE + 8 * 64);
;             const bf16x8 v0 = __builtin_shufflevector(a0, a1, 0, 1, 2, 3, 4, 5, 6, 7), v1 = __builtin_shufflevector(b0, b1, 0, 1, 2, 3, 4, 5, 6, 7);
;             o0 = __builtin_amdgcn_mfma_f32_32x32x16_bf16(v0, pa, o0, 0, 0, 0);
;             o1 = __builtin_amdgcn_mfma_f32_32x32x16_bf16(v1, pa, o1, 0, 0, 0);
;         }
;     }
.LBB0_940:
	v_pk_add_f32 v[220:221], v[36:37], v[164:165] op_sel:[0,1] op_sel_hi:[1,1] neg_lo:[0,1] neg_hi:[0,1]
	v_pk_add_f32 v[222:223], v[38:39], v[164:165] op_sel:[0,1] op_sel_hi:[1,1] neg_lo:[0,1] neg_hi:[0,1]
	v_pk_add_f32 v[224:225], v[40:41], v[164:165] op_sel:[0,1] op_sel_hi:[1,1] neg_lo:[0,1] neg_hi:[0,1]
	v_pk_add_f32 v[226:227], v[42:43], v[164:165] op_sel:[0,1] op_sel_hi:[1,1] neg_lo:[0,1] neg_hi:[0,1]
	v_pk_add_f32 v[228:229], v[44:45], v[164:165] op_sel:[0,1] op_sel_hi:[1,1] neg_lo:[0,1] neg_hi:[0,1]
	v_pk_add_f32 v[230:231], v[46:47], v[164:165] op_sel:[0,1] op_sel_hi:[1,1] neg_lo:[0,1] neg_hi:[0,1]
	v_pk_add_f32 v[232:233], v[48:49], v[164:165] op_sel:[0,1] op_sel_hi:[1,1] neg_lo:[0,1] neg_hi:[0,1]
	v_pk_add_f32 v[234:235], v[50:51], v[164:165] op_sel:[0,1] op_sel_hi:[1,1] neg_lo:[0,1] neg_hi:[0,1]
	v_add_u32_e32 v149, 0x1200, v149
	v_add_u32_e32 v167, 0x80, v167
	v_add_u32_e32 v244, 0x19800, v167
	ds_read2_b32 v[36:37], v244 offset1:1
	ds_read2_b32 v[38:39], v244 offset0:2 offset1:3
	ds_read2_b32 v[40:41], v244 offset0:8 offset1:9
	ds_read2_b32 v[42:43], v244 offset0:10 offset1:11
	v_add_u32_e32 v246, 0, v149
	ds_read_b128 v[236:239], v246
	ds_read2_b32 v[44:45], v244 offset0:16 offset1:17
	ds_read2_b32 v[46:47], v244 offset0:18 offset1:19
	ds_read2_b32 v[48:49], v244 offset0:24 offset1:25
	ds_read2_b32 v[50:51], v244 offset0:26 offset1:27
	ds_read_b128 v[240:243], v246 offset:32
	v_exp_f32_e32 v200, v220
	v_exp_f32_e32 v201, v221
	v_exp_f32_e32 v202, v222
	v_exp_f32_e32 v203, v223
	v_exp_f32_e32 v204, v224
	v_exp_f32_e32 v205, v225
	v_exp_f32_e32 v206, v226
	v_exp_f32_e32 v207, v227
	v_add_u32_e32 v184, 0, v135
	v_exp_f32_e32 v208, v228
	ds_read_b64_tr_b16 v[190:191], v184 offset:55296
	ds_read_b64_tr_b16 v[192:193], v184 offset:55808
	v_exp_f32_e32 v209, v229
	v_add_u32_e32 v245, 0x6000, v184
	v_exp_f32_e32 v210, v230
	ds_read_b64_tr_b16 v[194:195], v245 offset:55296
	ds_read_b64_tr_b16 v[196:197], v245 offset:55808
	ds_read_b64_tr_b16 v[168:169], v184 offset:56320
	ds_read_b64_tr_b16 v[170:171], v184 offset:56832
	v_exp_f32_e32 v211, v231
	v_exp_f32_e32 v212, v232
	v_cvt_pk_bf16_f32 v186, v200, v201
	v_cvt_pk_bf16_f32 v187, v202, v203
	v_cvt_pk_bf16_f32 v188, v204, v205
	v_cvt_pk_bf16_f32 v189, v206, v207
	s_waitcnt lgkmcnt(4)
	v_mfma_f32_32x32x16_bf16 v[20:35], v[190:193], v[186:189], v[20:35]
	v_exp_f32_e32 v213, v233
	ds_read_b64_tr_b16 v[190:191], v245 offset:56320
	ds_read_b64_tr_b16 v[192:193], v245 offset:56832
	s_waitcnt lgkmcnt(4)
	v_mfma_f32_32x32x16_bf16 v[4:19], v[194:197], v[186:189], v[4:19]
	v_exp_f32_e32 v214, v234
	v_exp_f32_e32 v215, v235
	v_cvt_pk_bf16_f32 v186, v208, v209
	v_cvt_pk_bf16_f32 v187, v210, v211
	v_cvt_pk_bf16_f32 v188, v212, v213
	v_cvt_pk_bf16_f32 v189, v214, v215
	s_waitcnt lgkmcnt(2)
	v_mfma_f32_32x32x16_bf16 v[20:35], v[168:171], v[186:189], v[20:35]
	s_add_i32 s6, s6, 1
	s_waitcnt lgkmcnt(0)
	v_mfma_f32_32x32x16_bf16 v[4:19], v[190:193], v[186:189], v[4:19]
	v_pk_add_f32 v[220:221], v[200:201], v[202:203]
	v_pk_add_f32 v[222:223], v[204:205], v[206:207]
	v_pk_add_f32 v[224:225], v[208:209], v[210:211]
	v_pk_add_f32 v[226:227], v[212:213], v[214:215]
	v_pk_add_f32 v[220:221], v[220:221], v[222:223]
	v_pk_add_f32 v[224:225], v[224:225], v[226:227]
	v_pk_add_f32 v[220:221], v[220:221], v[224:225]
	v_add_f32_e32 v220, v220, v221
	v_add_f32_e32 v3, v3, v220
	v_add_u32_e32 v135, 0x800, v135
	s_cmp_gt_u32 s6, 3
	s_cbranch_scc1 .LBB0_943
.LBB0_941:
	v_add_u32_e32 v176, 0, v149
	s_waitcnt vmcnt(17) lgkmcnt(1)
	v_mfma_f32_32x32x16_bf16 v[36:51], v[236:239], v[118:121], v[36:51]
	s_waitcnt vmcnt(16) lgkmcnt(0)
	v_mfma_f32_32x32x16_bf16 v[36:51], v[240:243], v[122:125], v[36:51]
	ds_read_b128 v[168:171], v176 offset:64
	ds_read_b128 v[172:175], v176 offset:96
	s_waitcnt vmcnt(15) lgkmcnt(1)
	v_mfma_f32_32x32x16_bf16 v[36:51], v[168:171], v[126:129], v[36:51]
	s_waitcnt vmcnt(14) lgkmcnt(0)
	v_mfma_f32_32x32x16_bf16 v[36:51], v[172:175], v[130:133], v[36:51]
	s_nop 11
	v_max3_f32 v168, v36, v37, v38
	v_max3_f32 v169, v39, v40, v41
	v_max3_f32 v170, v42, v43, v44
	v_max3_f32 v171, v45, v46, v47
	v_max3_f32 v172, v48, v49, v50
	v_max3_f32 v168, v168, v169, v51
	v_max3_f32 v170, v170, v171, v172
	v_max_f32_e32 v168, v168, v170
	v_mov_b32_e32 v169, v168
	s_nop 1
	v_permlane32_swap_b32_e32 v168, v169
	v_max_f32_e32 v168, v168, v169
	v_add_f32_e32 v169, 0x41000000, v165
	v_cmp_gt_f32_e32 vcc, v168, v169
	s_cbranch_vccz .LBB0_940
	v_max_f32_e32 v168, v168, v168
	v_max_f32_e32 v169, v165, v165
	v_max_f32_e32 v169, v169, v168
	v_sub_f32_e32 v165, v165, v169
	v_exp_f32_e32 v168, v165
	v_mov_b32_e32 v165, v169
	v_pk_mul_f32 v[34:35], v[34:35], v[168:169] op_sel_hi:[1,0]
	v_pk_mul_f32 v[32:33], v[32:33], v[168:169] op_sel_hi:[1,0]
	v_pk_mul_f32 v[30:31], v[30:31], v[168:169] op_sel_hi:[1,0]
	v_pk_mul_f32 v[28:29], v[28:29], v[168:169] op_sel_hi:[1,0]
	v_pk_mul_f32 v[26:27], v[26:27], v[168:169] op_sel_hi:[1,0]
	v_pk_mul_f32 v[24:25], v[24:25], v[168:169] op_sel_hi:[1,0]
	v_pk_mul_f32 v[22:23], v[22:23], v[168:169] op_sel_hi:[1,0]
	v_pk_mul_f32 v[20:21], v[20:21], v[168:169] op_sel_hi:[1,0]
	v_pk_mul_f32 v[18:19], v[18:19], v[168:169] op_sel_hi:[1,0]
	v_pk_mul_f32 v[16:17], v[16:17], v[168:169] op_sel_hi:[1,0]
	v_pk_mul_f32 v[14:15], v[14:15], v[168:169] op_sel_hi:[1,0]
	v_pk_mul_f32 v[12:13], v[12:13], v[168:169] op_sel_hi:[1,0]
	v_pk_mul_f32 v[10:11], v[10:11], v[168:169] op_sel_hi:[1,0]
	v_pk_mul_f32 v[8:9], v[8:9], v[168:169] op_sel_hi:[1,0]
	v_pk_mul_f32 v[6:7], v[6:7], v[168:169] op_sel_hi:[1,0]
	v_pk_mul_f32 v[4:5], v[4:5], v[168:169] op_sel_hi:[1,0]
	v_mul_f32_e32 v3, v3, v168
	s_branch .LBB0_940

; #define GAS __attribute__((address_space(1)))
; #define LAS __attribute__((address_space(3)))
; __device__ __forceinline__ void issue_loads(const UnitP& P, StageRegs& R, int tid) {
;     ...
;     const long qtok = (long)(P.mq0 + 32 * wave + r32) * P.dil + P.res;
; #pragma unroll
;     for (int s = 0; s < 4; ++s) R.q[s] = *(const GAS bf16x8*)(P.qg + qtok * P.qpitch + hi * 8 + 16 * s);
; template <bool BAND, int OUTMODE>
; __device__ __forceinline__ void compute(LAS unsigned char* lds, const bf16x8 (&qr)[4], int tid, int mq0, int dil, int res, int kt_min, int bias_tab, float sink2,
;                                         bf16* ob, int opitch, float* lsep) {
;     const int lane = tid & 63, wave = __builtin_amdgcn_readfirstlane(tid >> 6), r32 = lane & 31, hi = lane >> 5;
;     constexpr int NT = BAND ? 5 : 8;
;     const int kt0 = BAND ? wave : 0;
;     int t0 = BAND ? kt_min - kt0 : 0; t0 = t0 < 0 ? 0 : t0;
;     const LAS unsigned char* kb = lds + K_OFF + (32 * kt0 + r32) * KSTR + hi * 16;
;     const LAS float* bl = (const LAS float*)(lds + B_OFF) + bias_tab * BT_FLOATS + (31 - r32 + 4 * hi);
;     const int i16 = lane & 15, q4 = i16 >> 2, p4 = i16 & 3, blk16 = (lane >> 4) & 1;
;     const LAS unsigned char* vb = lds + V_OFF + (32 * kt0 + 4 * hi + q4) * 64 + blk16 * 32 + p4 * 8;
;     float mref = -1e20f, l = 0.f;
;     f32x16 o0, o1;
; #pragma unroll
;     for (int i = 0; i < 16; ++i) { o0[i] = 0.f; o1[i] = 0.f; }
.LBB0_949:
	s_or_b64 exec, exec, s[22:23]
	s_add_u32 s0, s34, s24
	s_addc_u32 s1, s35, 0
	v_add_u32_e32 v4, s37, v141
	s_add_u32 s4, s0, 0x9a00c00
	v_ashrrev_i32_e32 v5, 31, v4
	s_addc_u32 s5, s1, 0
	v_lshlrev_b64 v[4:5], 4, v[4:5]
	v_or_b32_e32 v4, s36, v4
	v_mov_b64_e32 v[6:7], s[4:5]
	v_mad_u64_u32 v[6:7], s[4:5], v4, s3, v[6:7]
	v_mad_i32_i24 v7, v5, s3, v7
	v_mov_b32_e32 v137, v3
	v_lshl_add_u64 v[4:5], v[6:7], 0, v[136:137]
	global_load_dwordx4 v[86:89], v[4:5], off
	global_load_dwordx4 v[90:93], v[4:5], off offset:32
	global_load_dwordx4 v[94:97], v[4:5], off offset:64
	global_load_dwordx4 v[98:101], v[4:5], off offset:96
	s_cmp_eq_u32 s31, 0
	v_readfirstlane_b32 s1, v0
	s_cselect_b32 s0, 4, 0
	s_lshr_b32 s1, s1, 6
	s_lshl_b32 s3, s1, 5
	s_sub_i32 s0, s0, s1
	v_or_b32_e32 v4, s3, v157
	s_max_i32 s0, s0, 0
	v_add_lshl_u32 v4, v4, v158, 6
	v_lshl_add_u32 v4, s0, 11, v4
	s_add_i32 s4, s0, -1
	v_or_b32_e32 v4, v4, v147
	s_mul_i32 s5, s0, 0x1200
	s_mulk_i32 s1, 0x1200
	s_lshl_b32 s0, s0, 7
	v_mov_b32_e32 v18, v3
	v_mov_b32_e32 v19, v3
	v_add_u32_e32 v137, v4, v148
	s_add_i32 s5, s5, s1
	s_add_i32 s0, s25, s0
	v_mov_b32_e32 v4, v3
	v_mov_b32_e32 v5, v3
	v_mov_b32_e32 v6, v3
	v_mov_b32_e32 v7, v3
	v_mov_b32_e32 v8, v3
	v_mov_b32_e32 v9, v3
	v_mov_b32_e32 v10, v3
	v_mov_b32_e32 v11, v3
	v_mov_b32_e32 v12, v3
	v_mov_b32_e32 v13, v3
	v_mov_b32_e32 v14, v3
	v_mov_b32_e32 v15, v3
	v_mov_b32_e32 v16, v3
	v_mov_b32_e32 v17, v3
	v_mov_b64_e32 v[34:35], v[18:19]
	v_add3_u32 v140, s5, v160, v134
	v_add3_u32 v141, s0, v134, v161
	v_mov_b32_e32 v65, 0xe0ad78ec
	v_mov_b64_e32 v[32:33], v[16:17]
	v_mov_b64_e32 v[30:31], v[14:15]
	v_mov_b64_e32 v[28:29], v[12:13]
	v_mov_b64_e32 v[26:27], v[10:11]
	v_mov_b64_e32 v[24:25], v[8:9]
	v_mov_b64_e32 v[22:23], v[6:7]
	v_mov_b64_e32 v[20:21], v[4:5]
	v_add_u32_e32 v244, 0x1a400, v141
	ds_read2_b32 v[36:37], v244 offset1:1
	ds_read2_b32 v[38:39], v244 offset0:2 offset1:3
	ds_read2_b32 v[40:41], v244 offset0:8 offset1:9
	ds_read2_b32 v[42:43], v244 offset0:10 offset1:11
	v_add_u32_e32 v246, 0, v140
	ds_read_b128 v[236:239], v246
	ds_read2_b32 v[44:45], v244 offset0:16 offset1:17
	ds_read2_b32 v[46:47], v244 offset0:18 offset1:19
	ds_read2_b32 v[48:49], v244 offset0:24 offset1:25
	ds_read2_b32 v[50:51], v244 offset0:26 offset1:27
	ds_read_b128 v[240:243], v246 offset:32
	s_branch .LBB0_951
; #define LAS __attribute__((address_space(3)))
; template <bool BAND, int OUTMODE>
; __device__ __forceinline__ void compute(LAS unsigned char* lds, const bf16x8 (&qr)[4], int tid, int mq0, int dil, int res, int kt_min, int bias_tab, float sink2,
;                                         bf16* ob, int opitch, float* lsep) {
;     ...
;     for (int t = t0; t < NT; ++t) {
;         f32x16 S;
;         if (BAND) {
; #pragma unroll
;             for (int i = 0; i < 16; ++i) S[i] = bl[32 * t + (i & 3) + 8 * (i >> 2)];
;         } else {
; #pragma unroll
;             for (int i = 0; i < 16; ++i) S[i] = 0.f;
;         }
; #pragma unroll
;         for (int s = 0; s < 4; ++s) { const bf16x8 kf = *(const LAS bf16x8*)(kb + t * 32 * KSTR + s * 32); S = __builtin_amdgcn_mfma_f32_32x32x16_bf16(kf, qr[s], S, 0, 0, 0); }
;         float m0 = fmaxf(fmaxf(S[0], S[1]), fmaxf(S[2], S[3])), m1 = fmaxf(fmaxf(S[4], S[5]), fmaxf(S[6], S[7])), m2 = fmaxf(fmaxf(S[8], S[9]), fmaxf(S[10], S[11])), m3 = fmaxf(fmaxf(S[12], S[13]), fmaxf(S[14], S[15]));
;         const float mt = xhalf_max(fmaxf(fmaxf(m0, m1), fmaxf(m2, m3)));
;         if (__any(mt > mref + THR)) {
;             const float mnew = fmaxf(mref, mt), f = __builtin_amdgcn_exp2f(mref - mnew);
;             mref = mnew; l *= f;
; #pragma unroll
;             for (int i = 0; i < 16; ++i) { o0[i] *= f; o1[i] *= f; }
;         }
; #pragma unroll
;         for (int i = 0; i < 16; ++i) { const float p = __builtin_amdgcn_exp2f(S[i] - mref); S[i] = p; l += p; }
; #pragma unroll
;         for (int s = 0; s < 2; ++s) {
;             v4u pw; pw.x = cvtpk(S[8 * s + 0], S[8 * s + 1]); pw.y = cvtpk(S[8 * s + 2], S[8 * s + 3]); pw.z = cvtpk(S[8 * s + 4], S[8 * s + 5]); pw.w = cvtpk(S[8 * s + 6], S[8 * s + 7]);
;             const bf16x8 pa = __builtin_bit_cast(bf16x8, pw);
;             const LAS unsigned char* vp = vb + (32 * t + 16 * s) * 64;
;             const s16x4 a0 = vtr(vp), a1 = vtr(vp + 8 * 64), b0 = vtr(vp + VPLANE), b1 = vtr(vp + VPLANE + 8 * 64);
;             const bf16x8 v0 = __builtin_shufflevector(a0, a1, 0, 1, 2, 3, 4, 5, 6, 7), v1 = __builtin_shufflevector(b0, b1, 0, 1, 2, 3, 4, 5, 6, 7);
;             o0 = __builtin_amdgcn_mfma_f32_32x32x16_bf16(v0, pa, o0, 0, 0, 0);
;             o1 = __builtin_amdgcn_mfma_f32_32x32x16_bf16(v1, pa, o1, 0, 0, 0);
;         }
;     }
.LBB0_950:
	v_pk_add_f32 v[220:221], v[36:37], v[64:65] op_sel:[0,1] op_sel_hi:[1,1] neg_lo:[0,1] neg_hi:[0,1]
	v_pk_add_f32 v[222:223], v[38:39], v[64:65] op_sel:[0,1] op_sel_hi:[1,1] neg_lo:[0,1] neg_hi:[0,1]
	v_pk_add_f32 v[224:225], v[40:41], v[64:65] op_sel:[0,1] op_sel_hi:[1,1] neg_lo:[0,1] neg_hi:[0,1]
	v_pk_add_f32 v[226:227], v[42:43], v[64:65] op_sel:[0,1] op_sel_hi:[1,1] neg_lo:[0,1] neg_hi:[0,1]
	v_pk_add_f32 v[228:229], v[44:45], v[64:65] op_sel:[0,1] op_sel_hi:[1,1] neg_lo:[0,1] neg_hi:[0,1]
	v_pk_add_f32 v[230:231], v[46:47], v[64:65] op_sel:[0,1] op_sel_hi:[1,1] neg_lo:[0,1] neg_hi:[0,1]
	v_pk_add_f32 v[232:233], v[48:49], v[64:65] op_sel:[0,1] op_sel_hi:[1,1] neg_lo:[0,1] neg_hi:[0,1]
	v_pk_add_f32 v[234:235], v[50:51], v[64:65] op_sel:[0,1] op_sel_hi:[1,1] neg_lo:[0,1] neg_hi:[0,1]
	v_add_u32_e32 v140, 0x1200, v140
	v_add_u32_e32 v141, 0x80, v141
	v_add_u32_e32 v244, 0x1a400, v141
	ds_read2_b32 v[36:37], v244 offset1:1
	ds_read2_b32 v[38:39], v244 offset0:2 offset1:3
	ds_read2_b32 v[40:41], v244 offset0:8 offset1:9
	ds_read2_b32 v[42:43], v244 offset0:10 offset1:11
	v_add_u32_e32 v246, 0, v140
	ds_read_b128 v[236:239], v246
	ds_read2_b32 v[44:45], v244 offset0:16 offset1:17
	ds_read2_b32 v[46:47], v244 offset0:18 offset1:19
	ds_read2_b32 v[48:49], v244 offset0:24 offset1:25
	ds_read2_b32 v[50:51], v244 offset0:26 offset1:27
	ds_read_b128 v[240:243], v246 offset:32
	v_exp_f32_e32 v200, v220
	v_exp_f32_e32 v201, v221
	v_exp_f32_e32 v202, v222
	v_exp_f32_e32 v203, v223
	v_exp_f32_e32 v204, v224
	v_exp_f32_e32 v205, v225
	v_exp_f32_e32 v206, v226
	v_exp_f32_e32 v207, v227
	v_add_u32_e32 v182, 0, v137
	v_exp_f32_e32 v208, v228
	ds_read_b64_tr_b16 v[190:191], v182 offset:55296
	ds_read_b64_tr_b16 v[192:193], v182 offset:55808
	v_exp_f32_e32 v209, v229
	v_add_u32_e32 v245, 0x6000, v182
	v_exp_f32_e32 v210, v230
	ds_read_b64_tr_b16 v[194:195], v245 offset:55296
	ds_read_b64_tr_b16 v[196:197], v245 offset:55808
	ds_read_b64_tr_b16 v[166:167], v182 offset:56320
	ds_read_b64_tr_b16 v[168:169], v182 offset:56832
	v_exp_f32_e32 v211, v231
	v_exp_f32_e32 v212, v232
	v_cvt_pk_bf16_f32 v186, v200, v201
	v_cvt_pk_bf16_f32 v187, v202, v203
	v_cvt_pk_bf16_f32 v188, v204, v205
	v_cvt_pk_bf16_f32 v189, v206, v207
	s_waitcnt lgkmcnt(4)
	v_mfma_f32_32x32x16_bf16 v[20:35], v[190:193], v[186:189], v[20:35]
	v_exp_f32_e32 v213, v233
	ds_read_b64_tr_b16 v[190:191], v245 offset:56320
	ds_read_b64_tr_b16 v[192:193], v245 offset:56832
	s_waitcnt lgkmcnt(4)
	v_mfma_f32_32x32x16_bf16 v[4:19], v[194:197], v[186:189], v[4:19]
	v_exp_f32_e32 v214, v234
	v_exp_f32_e32 v215, v235
	v_cvt_pk_bf16_f32 v186, v208, v209
	v_cvt_pk_bf16_f32 v187, v210, v211
	v_cvt_pk_bf16_f32 v188, v212, v213
	v_cvt_pk_bf16_f32 v189, v214, v215
	s_waitcnt lgkmcnt(2)
	v_mfma_f32_32x32x16_bf16 v[20:35], v[166:169], v[186:189], v[20:35]
	s_add_i32 s4, s4, 1
	s_waitcnt lgkmcnt(0)
	v_mfma_f32_32x32x16_bf16 v[4:19], v[190:193], v[186:189], v[4:19]
	v_pk_add_f32 v[220:221], v[200:201], v[202:203]
	v_pk_add_f32 v[222:223], v[204:205], v[206:207]
	v_pk_add_f32 v[224:225], v[208:209], v[210:211]
	v_pk_add_f32 v[226:227], v[212:213], v[214:215]
	v_pk_add_f32 v[220:221], v[220:221], v[222:223]
	v_pk_add_f32 v[224:225], v[224:225], v[226:227]
	v_pk_add_f32 v[220:221], v[220:221], v[224:225]
	v_add_f32_e32 v220, v220, v221
	v_add_f32_e32 v3, v3, v220
	v_add_u32_e32 v137, 0x800, v137
	s_cmp_lt_u32 s4, 4
	s_cbranch_scc0 .LBB0_953
.LBB0_951:
	v_add_u32_e32 v174, 0, v140
	s_waitcnt vmcnt(21) lgkmcnt(1)
	v_mfma_f32_32x32x16_bf16 v[36:51], v[236:239], v[60:63], v[36:51]
	s_waitcnt vmcnt(20) lgkmcnt(0)
	v_mfma_f32_32x32x16_bf16 v[36:51], v[240:243], v[74:77], v[36:51]
	ds_read_b128 v[166:169], v174 offset:64
	ds_read_b128 v[170:173], v174 offset:96
	s_waitcnt vmcnt(19) lgkmcnt(1)
	v_mfma_f32_32x32x16_bf16 v[36:51], v[166:169], v[78:81], v[36:51]
	s_waitcnt vmcnt(18) lgkmcnt(0)
	v_mfma_f32_32x32x16_bf16 v[36:51], v[170:173], v[82:85], v[36:51]
	s_nop 11
	v_max3_f32 v166, v36, v37, v38
	v_max3_f32 v167, v39, v40, v41
	v_max3_f32 v168, v42, v43, v44
	v_max3_f32 v169, v45, v46, v47
	v_max3_f32 v170, v48, v49, v50
	v_max3_f32 v166, v166, v167, v51
	v_max3_f32 v168, v168, v169, v170
	v_max_f32_e32 v166, v166, v168
	v_mov_b32_e32 v167, v166
	s_nop 1
	v_permlane32_swap_b32_e32 v166, v167
	v_max_f32_e32 v166, v166, v167
	v_add_f32_e32 v167, 0x41000000, v65
	v_cmp_gt_f32_e32 vcc, v166, v167
	s_cbranch_vccz .LBB0_950
	v_max_f32_e32 v166, v166, v166
	v_max_f32_e32 v167, v65, v65
	v_max_f32_e32 v167, v167, v166
	v_sub_f32_e32 v65, v65, v167
	v_exp_f32_e32 v166, v65
	v_mov_b32_e32 v65, v167
	v_pk_mul_f32 v[34:35], v[34:35], v[166:167] op_sel_hi:[1,0]
	v_pk_mul_f32 v[32:33], v[32:33], v[166:167] op_sel_hi:[1,0]
	v_pk_mul_f32 v[30:31], v[30:31], v[166:167] op_sel_hi:[1,0]
	v_pk_mul_f32 v[28:29], v[28:29], v[166:167] op_sel_hi:[1,0]
	v_pk_mul_f32 v[26:27], v[26:27], v[166:167] op_sel_hi:[1,0]
	v_pk_mul_f32 v[24:25], v[24:25], v[166:167] op_sel_hi:[1,0]
	v_pk_mul_f32 v[22:23], v[22:23], v[166:167] op_sel_hi:[1,0]
	v_pk_mul_f32 v[20:21], v[20:21], v[166:167] op_sel_hi:[1,0]
	v_pk_mul_f32 v[18:19], v[18:19], v[166:167] op_sel_hi:[1,0]
	v_pk_mul_f32 v[16:17], v[16:17], v[166:167] op_sel_hi:[1,0]
	v_pk_mul_f32 v[14:15], v[14:15], v[166:167] op_sel_hi:[1,0]
	v_pk_mul_f32 v[12:13], v[12:13], v[166:167] op_sel_hi:[1,0]
	v_pk_mul_f32 v[10:11], v[10:11], v[166:167] op_sel_hi:[1,0]
	v_pk_mul_f32 v[8:9], v[8:9], v[166:167] op_sel_hi:[1,0]
	v_pk_mul_f32 v[6:7], v[6:7], v[166:167] op_sel_hi:[1,0]
	v_pk_mul_f32 v[4:5], v[4:5], v[166:167] op_sel_hi:[1,0]
	v_mul_f32_e32 v3, v3, v166
	s_branch .LBB0_950

; #define GAS __attribute__((address_space(1)))
; #define LAS __attribute__((address_space(3)))
; __device__ __forceinline__ void issue_loads(const UnitP& P, StageRegs& R, int tid) {
;     ...
;     const long qtok = (long)(P.mq0 + 32 * wave + r32) * P.dil + P.res;
; #pragma unroll
;     for (int s = 0; s < 4; ++s) R.q[s] = *(const GAS bf16x8*)(P.qg + qtok * P.qpitch + hi * 8 + 16 * s);
; template <bool BAND, int OUTMODE>
; __device__ __forceinline__ void compute(LAS unsigned char* lds, const bf16x8 (&qr)[4], int tid, int mq0, int dil, int res, int kt_min, int bias_tab, float sink2,
;                                         bf16* ob, int opitch, float* lsep) {
;     const int lane = tid & 63, wave = __builtin_amdgcn_readfirstlane(tid >> 6), r32 = lane & 31, hi = lane >> 5;
;     constexpr int NT = BAND ? 5 : 8;
;     const int kt0 = BAND ? wave : 0;
;     int t0 = BAND ? kt_min - kt0 : 0; t0 = t0 < 0 ? 0 : t0;
;     const LAS unsigned char* kb = lds + K_OFF + (32 * kt0 + r32) * KSTR + hi * 16;
;     const LAS float* bl = (const LAS float*)(lds + B_OFF) + bias_tab * BT_FLOATS + (31 - r32 + 4 * hi);
;     const int i16 = lane & 15, q4 = i16 >> 2, p4 = i16 & 3, blk16 = (lane >> 4) & 1;
;     const LAS unsigned char* vb = lds + V_OFF + (32 * kt0 + 4 * hi + q4) * 64 + blk16 * 32 + p4 * 8;
;     float mref = -1e20f, l = 0.f;
;     f32x16 o0, o1;
; #pragma unroll
;     for (int i = 0; i < 16; ++i) { o0[i] = 0.f; o1[i] = 0.f; }
.LBB0_959:
	s_or_b64 exec, exec, s[22:23]
	s_add_u32 s4, s34, s24
	s_addc_u32 s5, s35, 0
	v_lshl_add_u64 v[4:5], s[4:5], 0, v[138:139]
	v_mov_b32_e32 v137, v3
	v_lshl_add_u64 v[4:5], v[4:5], 0, v[136:137]
	s_mov_b64 s[4:5], 0x9a01200
	v_lshl_add_u64 v[6:7], v[4:5], 0, s[4:5]
	v_add_co_u32_e32 v4, vcc, 0x9a01000, v4
	s_cmp_eq_u32 s37, 0
	s_nop 0
	v_addc_co_u32_e32 v5, vcc, 0, v5, vcc
	global_load_dwordx4 v[74:77], v[6:7], off offset:32
	global_load_dwordx4 v[78:81], v[6:7], off offset:64
	global_load_dwordx4 v[82:85], v[4:5], off offset:512
	global_load_dwordx4 v[102:105], v[6:7], off offset:96
	v_readfirstlane_b32 s1, v0
	s_cselect_b32 s0, 4, 0
	s_lshr_b32 s1, s1, 6
	s_lshl_b32 s3, s1, 5
	s_sub_i32 s0, s0, s1
	v_or_b32_e32 v2, s3, v157
	s_max_i32 s0, s0, 0
	v_add_lshl_u32 v2, v2, v158, 6
	v_lshl_add_u32 v2, s0, 11, v2
	s_add_i32 s4, s0, -1
	v_or_b32_e32 v2, v2, v147
	s_mul_i32 s5, s0, 0x1200
	s_mulk_i32 s1, 0x1200
	s_lshl_b32 s0, s0, 7
	v_mov_b32_e32 v16, v3
	v_mov_b32_e32 v17, v3
	v_add_u32_e32 v131, v2, v148
	s_add_i32 s5, s5, s1
	s_add_i32 s25, s25, s0
	v_mov_b32_e32 v2, v3
	v_mov_b32_e32 v4, v3
	v_mov_b32_e32 v5, v3
	v_mov_b32_e32 v6, v3
	v_mov_b32_e32 v7, v3
	v_mov_b32_e32 v8, v3
	v_mov_b32_e32 v9, v3
	v_mov_b32_e32 v10, v3
	v_mov_b32_e32 v11, v3
	v_mov_b32_e32 v12, v3
	v_mov_b32_e32 v13, v3
	v_mov_b32_e32 v14, v3
	v_mov_b32_e32 v15, v3
	v_mov_b64_e32 v[32:33], v[16:17]
	v_mov_b64_e32 v[48:49], v[16:17]
	v_add3_u32 v132, s5, v160, v134
	v_add3_u32 v133, s25, v134, v161
	v_mov_b32_e32 v130, 0xe0ad78ec
	v_mov_b64_e32 v[30:31], v[14:15]
	v_mov_b64_e32 v[28:29], v[12:13]
	v_mov_b64_e32 v[26:27], v[10:11]
	v_mov_b64_e32 v[24:25], v[8:9]
	v_mov_b64_e32 v[22:23], v[6:7]
	v_mov_b64_e32 v[20:21], v[4:5]
	v_mov_b64_e32 v[18:19], v[2:3]
	v_mov_b64_e32 v[46:47], v[14:15]
	v_mov_b64_e32 v[44:45], v[12:13]
	v_mov_b64_e32 v[42:43], v[10:11]
	v_mov_b64_e32 v[40:41], v[8:9]
	v_mov_b64_e32 v[38:39], v[6:7]
	v_mov_b64_e32 v[36:37], v[4:5]
	v_mov_b64_e32 v[34:35], v[2:3]
	v_add_u32_e32 v244, 0x1b000, v133
	ds_read2_b32 v[50:51], v244 offset1:1
	ds_read2_b32 v[52:53], v244 offset0:2 offset1:3
	ds_read2_b32 v[54:55], v244 offset0:8 offset1:9
	ds_read2_b32 v[56:57], v244 offset0:10 offset1:11
	v_add_u32_e32 v246, 0, v132
	ds_read_b128 v[236:239], v246
	ds_read2_b32 v[58:59], v244 offset0:16 offset1:17
	ds_read2_b32 v[60:61], v244 offset0:18 offset1:19
	ds_read2_b32 v[62:63], v244 offset0:24 offset1:25
	ds_read2_b32 v[64:65], v244 offset0:26 offset1:27
	ds_read_b128 v[240:243], v246 offset:32
	s_branch .LBB0_961
; #define LAS __attribute__((address_space(3)))
; template <bool BAND, int OUTMODE>
; __device__ __forceinline__ void compute(LAS unsigned char* lds, const bf16x8 (&qr)[4], int tid, int mq0, int dil, int res, int kt_min, int bias_tab, float sink2,
;                                         bf16* ob, int opitch, float* lsep) {
;     ...
;     for (int t = t0; t < NT; ++t) {
;         f32x16 S;
;         if (BAND) {
; #pragma unroll
;             for (int i = 0; i < 16; ++i) S[i] = bl[32 * t + (i & 3) + 8 * (i >> 2)];
;         } else {
; #pragma unroll
;             for (int i = 0; i < 16; ++i) S[i] = 0.f;
;         }
; #pragma unroll
;         for (int s = 0; s < 4; ++s) { const bf16x8 kf = *(const LAS bf16x8*)(kb + t * 32 * KSTR + s * 32); S = __builtin_amdgcn_mfma_f32_32x32x16_bf16(kf, qr[s], S, 0, 0, 0); }
;         float m0 = fmaxf(fmaxf(S[0], S[1]), fmaxf(S[2], S[3])), m1 = fmaxf(fmaxf(S[4], S[5]), fmaxf(S[6], S[7])), m2 = fmaxf(fmaxf(S[8], S[9]), fmaxf(S[10], S[11])), m3 = fmaxf(fmaxf(S[12], S[13]), fmaxf(S[14], S[15]));
;         const float mt = xhalf_max(fmaxf(fmaxf(m0, m1), fmaxf(m2, m3)));
;         if (__any(mt > mref + THR)) {
;             const float mnew = fmaxf(mref, mt), f = __builtin_amdgcn_exp2f(mref - mnew);
;             mref = mnew; l *= f;
; #pragma unroll
;             for (int i = 0; i < 16; ++i) { o0[i] *= f; o1[i] *= f; }
;         }
; #pragma unroll
;         for (int i = 0; i < 16; ++i) { const float p = __builtin_amdgcn_exp2f(S[i] - mref); S[i] = p; l += p; }
; #pragma unroll
;         for (int s = 0; s < 2; ++s) {
;             v4u pw; pw.x = cvtpk(S[8 * s + 0], S[8 * s + 1]); pw.y = cvtpk(S[8 * s + 2], S[8 * s + 3]); pw.z = cvtpk(S[8 * s + 4], S[8 * s + 5]); pw.w = cvtpk(S[8 * s + 6], S[8 * s + 7]);
;             const bf16x8 pa = __builtin_bit_cast(bf16x8, pw);
;             const LAS unsigned char* vp = vb + (32 * t + 16 * s) * 64;
;             const s16x4 a0 = vtr(vp), a1 = vtr(vp + 8 * 64), b0 = vtr(vp + VPLANE), b1 = vtr(vp + VPLANE + 8 * 64);
;             const bf16x8 v0 = __builtin_shufflevector(a0, a1, 0, 1, 2, 3, 4, 5, 6, 7), v1 = __builtin_shufflevector(b0, b1, 0, 1, 2, 3, 4, 5, 6, 7);
;             o0 = __builtin_amdgcn_mfma_f32_32x32x16_bf16(v0, pa, o0, 0, 0, 0);
;             o1 = __builtin_amdgcn_mfma_f32_32x32x16_bf16(v1, pa, o1, 0, 0, 0);
;         }
;     }
.LBB0_960:
	v_pk_add_f32 v[220:221], v[50:51], v[130:131] op_sel_hi:[1,0] neg_lo:[0,1] neg_hi:[0,1]
	v_pk_add_f32 v[222:223], v[52:53], v[130:131] op_sel_hi:[1,0] neg_lo:[0,1] neg_hi:[0,1]
	v_pk_add_f32 v[224:225], v[54:55], v[130:131] op_sel_hi:[1,0] neg_lo:[0,1] neg_hi:[0,1]
	v_pk_add_f32 v[226:227], v[56:57], v[130:131] op_sel_hi:[1,0] neg_lo:[0,1] neg_hi:[0,1]
	v_pk_add_f32 v[228:229], v[58:59], v[130:131] op_sel_hi:[1,0] neg_lo:[0,1] neg_hi:[0,1]
	v_pk_add_f32 v[230:231], v[60:61], v[130:131] op_sel_hi:[1,0] neg_lo:[0,1] neg_hi:[0,1]
	v_pk_add_f32 v[232:233], v[62:63], v[130:131] op_sel_hi:[1,0] neg_lo:[0,1] neg_hi:[0,1]
	v_pk_add_f32 v[234:235], v[64:65], v[130:131] op_sel_hi:[1,0] neg_lo:[0,1] neg_hi:[0,1]
	v_add_u32_e32 v132, 0x1200, v132
	v_add_u32_e32 v133, 0x80, v133
	v_add_u32_e32 v244, 0x1b000, v133
	ds_read2_b32 v[50:51], v244 offset1:1
	ds_read2_b32 v[52:53], v244 offset0:2 offset1:3
	ds_read2_b32 v[54:55], v244 offset0:8 offset1:9
	ds_read2_b32 v[56:57], v244 offset0:10 offset1:11
	v_add_u32_e32 v246, 0, v132
	ds_read_b128 v[236:239], v246
	ds_read2_b32 v[58:59], v244 offset0:16 offset1:17
	ds_read2_b32 v[60:61], v244 offset0:18 offset1:19
	ds_read2_b32 v[62:63], v244 offset0:24 offset1:25
	ds_read2_b32 v[64:65], v244 offset0:26 offset1:27
	ds_read_b128 v[240:243], v246 offset:32
	v_exp_f32_e32 v201, v221
	v_exp_f32_e32 v202, v222
	v_exp_f32_e32 v203, v223
	v_exp_f32_e32 v204, v224
	v_exp_f32_e32 v205, v225
	v_exp_f32_e32 v206, v226
	v_exp_f32_e32 v207, v227
	v_add_u32_e32 v137, 0, v131
	v_exp_f32_e32 v200, v220
	v_exp_f32_e32 v208, v228
	ds_read_b64_tr_b16 v[8:9], v137 offset:55296
	ds_read_b64_tr_b16 v[10:11], v137 offset:55808
	v_exp_f32_e32 v209, v229
	v_add_u32_e32 v245, 0x6000, v137
	v_exp_f32_e32 v210, v230
	ds_read_b64_tr_b16 v[12:13], v245 offset:55296
	ds_read_b64_tr_b16 v[14:15], v245 offset:55808
	ds_read_b64_tr_b16 v[186:187], v137 offset:56320
	ds_read_b64_tr_b16 v[188:189], v137 offset:56832
	v_exp_f32_e32 v211, v231
	v_exp_f32_e32 v212, v232
	v_cvt_pk_bf16_f32 v4, v200, v201
	v_cvt_pk_bf16_f32 v5, v202, v203
	v_cvt_pk_bf16_f32 v6, v204, v205
	v_cvt_pk_bf16_f32 v7, v206, v207
	s_waitcnt lgkmcnt(4)
	v_mfma_f32_32x32x16_bf16 v[34:49], v[8:11], v[4:7], v[34:49]
	v_exp_f32_e32 v213, v233
	ds_read_b64_tr_b16 v[8:9], v245 offset:56320
	ds_read_b64_tr_b16 v[10:11], v245 offset:56832
	s_waitcnt lgkmcnt(4)
	v_mfma_f32_32x32x16_bf16 v[18:33], v[12:15], v[4:7], v[18:33]
	v_exp_f32_e32 v214, v234
	v_exp_f32_e32 v215, v235
	v_cvt_pk_bf16_f32 v4, v208, v209
	v_cvt_pk_bf16_f32 v5, v210, v211
	v_cvt_pk_bf16_f32 v6, v212, v213
	v_cvt_pk_bf16_f32 v7, v214, v215
	s_waitcnt lgkmcnt(2)
	v_mfma_f32_32x32x16_bf16 v[34:49], v[186:189], v[4:7], v[34:49]
	s_add_i32 s4, s4, 1
	s_waitcnt lgkmcnt(0)
	v_mfma_f32_32x32x16_bf16 v[18:33], v[8:11], v[4:7], v[18:33]
	v_pk_add_f32 v[220:221], v[200:201], v[202:203]
	v_pk_add_f32 v[222:223], v[204:205], v[206:207]
	v_pk_add_f32 v[224:225], v[208:209], v[210:211]
	v_pk_add_f32 v[226:227], v[212:213], v[214:215]
	v_pk_add_f32 v[220:221], v[220:221], v[222:223]
	v_pk_add_f32 v[224:225], v[224:225], v[226:227]
	v_pk_add_f32 v[220:221], v[220:221], v[224:225]
	v_add_f32_e32 v220, v220, v221
	v_add_f32_e32 v3, v3, v220
	v_add_u32_e32 v131, 0x800, v131
	s_cmp_lt_u32 s4, 4
	s_cbranch_scc0 .LBB0_963
.LBB0_961:
	v_add_u32_e32 v12, 0, v132
	s_waitcnt vmcnt(17) lgkmcnt(1)
	v_mfma_f32_32x32x16_bf16 v[50:65], v[236:239], v[86:89], v[50:65]
	s_waitcnt vmcnt(16) lgkmcnt(0)
	v_mfma_f32_32x32x16_bf16 v[50:65], v[240:243], v[90:93], v[50:65]
	ds_read_b128 v[4:7], v12 offset:64
	ds_read_b128 v[8:11], v12 offset:96
	s_waitcnt vmcnt(15) lgkmcnt(1)
	v_mfma_f32_32x32x16_bf16 v[50:65], v[4:7], v[94:97], v[50:65]
	s_waitcnt vmcnt(14) lgkmcnt(0)
	v_mfma_f32_32x32x16_bf16 v[50:65], v[8:11], v[98:101], v[50:65]
	s_nop 11
	v_max3_f32 v2, v50, v51, v52
	v_max3_f32 v4, v53, v54, v55
	v_max3_f32 v5, v56, v57, v58
	v_max3_f32 v6, v59, v60, v61
	v_max3_f32 v7, v62, v63, v64
	v_max3_f32 v2, v2, v4, v65
	v_max3_f32 v5, v5, v6, v7
	v_max_f32_e32 v2, v2, v5
	v_mov_b32_e32 v4, v2
	s_nop 1
	v_permlane32_swap_b32_e32 v2, v4
	v_max_f32_e32 v2, v2, v4
	v_add_f32_e32 v4, 0x41000000, v130
	v_cmp_gt_f32_e32 vcc, v2, v4
	s_cbranch_vccz .LBB0_960
	v_max_f32_e32 v2, v2, v2
	v_max_f32_e32 v4, v130, v130
	v_max_f32_e32 v4, v4, v2
	v_sub_f32_e32 v2, v130, v4
	v_exp_f32_e32 v2, v2
	v_mov_b32_e32 v130, v4
	v_pk_mul_f32 v[48:49], v[48:49], v[2:3] op_sel_hi:[1,0]
	v_pk_mul_f32 v[46:47], v[46:47], v[2:3] op_sel_hi:[1,0]
	v_pk_mul_f32 v[44:45], v[44:45], v[2:3] op_sel_hi:[1,0]
	v_pk_mul_f32 v[42:43], v[42:43], v[2:3] op_sel_hi:[1,0]
	v_pk_mul_f32 v[40:41], v[40:41], v[2:3] op_sel_hi:[1,0]
	v_pk_mul_f32 v[38:39], v[38:39], v[2:3] op_sel_hi:[1,0]
	v_pk_mul_f32 v[36:37], v[36:37], v[2:3] op_sel_hi:[1,0]
	v_pk_mul_f32 v[34:35], v[34:35], v[2:3] op_sel_hi:[1,0]
	v_pk_mul_f32 v[32:33], v[32:33], v[2:3] op_sel_hi:[1,0]
	v_pk_mul_f32 v[30:31], v[30:31], v[2:3] op_sel_hi:[1,0]
	v_pk_mul_f32 v[28:29], v[28:29], v[2:3] op_sel_hi:[1,0]
	v_pk_mul_f32 v[26:27], v[26:27], v[2:3] op_sel_hi:[1,0]
	v_pk_mul_f32 v[24:25], v[24:25], v[2:3] op_sel_hi:[1,0]
	v_pk_mul_f32 v[22:23], v[22:23], v[2:3] op_sel_hi:[1,0]
	v_pk_mul_f32 v[20:21], v[20:21], v[2:3] op_sel_hi:[1,0]
	v_pk_mul_f32 v[18:19], v[18:19], v[2:3] op_sel_hi:[1,0]
	v_mul_f32_e32 v3, v3, v2
	s_branch .LBB0_960

; template <bool BAND, int OUTMODE>
; __device__ __forceinline__ void compute(LAS unsigned char* lds, const bf16x8 (&qr)[4], int tid, int mq0, int dil, int res, int kt_min, int bias_tab, float sink2,
;                                         bf16* ob, int opitch, float* lsep) {
;     ...
;     const LAS unsigned char* kb = lds + K_OFF + (32 * kt0 + r32) * KSTR + hi * 16;
;     const LAS float* bl = (const LAS float*)(lds + B_OFF) + bias_tab * BT_FLOATS + (31 - r32 + 4 * hi);
;     const int i16 = lane & 15, q4 = i16 >> 2, p4 = i16 & 3, blk16 = (lane >> 4) & 1;
;     const LAS unsigned char* vb = lds + V_OFF + (32 * kt0 + 4 * hi + q4) * 64 + blk16 * 32 + p4 * 8;
;     float mref = -1e20f, l = 0.f;
;     f32x16 o0, o1;
; #pragma unroll
;     for (int i = 0; i < 16; ++i) { o0[i] = 0.f; o1[i] = 0.f; }
; #pragma unroll 1
;     for (int t = t0; t < NT; ++t) {
;         f32x16 S;
;         if (BAND) {
; #pragma unroll
;             for (int i = 0; i < 16; ++i) S[i] = bl[32 * t + (i & 3) + 8 * (i >> 2)];
;         } else {
; #pragma unroll
;             for (int i = 0; i < 16; ++i) S[i] = 0.f;
;         }
; #pragma unroll
;         for (int s = 0; s < 4; ++s) { const bf16x8 kf = *(const LAS bf16x8*)(kb + t * 32 * KSTR + s * 32); S = __builtin_amdgcn_mfma_f32_32x32x16_bf16(kf, qr[s], S, 0, 0, 0); }
;         float m0 = fmaxf(fmaxf(S[0], S[1]), fmaxf(S[2], S[3])), m1 = fmaxf(fmaxf(S[4], S[5]), fmaxf(S[6], S[7])), m2 = fmaxf(fmaxf(S[8], S[9]), fmaxf(S[10], S[11])), m3 = fmaxf(fmaxf(S[12], S[13]), fmaxf(S[14], S[15]));
;         const float mt = xhalf_max(fmaxf(fmaxf(m0, m1), fmaxf(m2, m3)));
;         if (__any(mt > mref + THR)) {
;             const float mnew = fmaxf(mref, mt), f = __builtin_amdgcn_exp2f(mref - mnew);
;             mref = mnew; l *= f;
; #pragma unroll
;             for (int i = 0; i < 16; ++i) { o0[i] *= f; o1[i] *= f; }
;         }
; #pragma unroll
;         for (int i = 0; i < 16; ++i) { const float p = __builtin_amdgcn_exp2f(S[i] - mref); S[i] = p; l += p; }
; #pragma unroll
;         for (int s = 0; s < 2; ++s) {
;             v4u pw; pw.x = cvtpk(S[8 * s + 0], S[8 * s + 1]); pw.y = cvtpk(S[8 * s + 2], S[8 * s + 3]); pw.z = cvtpk(S[8 * s + 4], S[8 * s + 5]); pw.w = cvtpk(S[8 * s + 6], S[8 * s + 7]);
;             const bf16x8 pa = __builtin_bit_cast(bf16x8, pw);
;             const LAS unsigned char* vp = vb + (32 * t + 16 * s) * 64;
.LBB0_967:
	s_or_b64 exec, exec, s[10:11]
	v_mov_b32_e32 v34, 0
	v_mul_u32_u24_e32 v2, 0xf0, v146
	v_and_b32_e32 v1, 0xc0, v1
	s_waitcnt lgkmcnt(0)
	s_barrier
	v_mov_b32_e32 v35, v34
	s_movk_i32 s0, 0x90
	v_add3_u32 v1, v2, v1, v147
	v_mov_b32_e32 v36, v34
	v_mov_b32_e32 v37, v34
	v_mov_b32_e32 v38, v34
	v_mov_b32_e32 v39, v34
	v_mov_b32_e32 v40, v34
	v_mov_b32_e32 v41, v34
	v_mov_b32_e32 v42, v34
	v_mov_b32_e32 v43, v34
	v_mov_b32_e32 v44, v34
	v_mov_b32_e32 v45, v34
	v_mov_b32_e32 v46, v34
	v_mov_b32_e32 v47, v34
	v_mov_b32_e32 v48, v34
	v_mov_b32_e32 v49, v34
	v_mov_b64_e32 v[2:3], v[34:35]
	v_mov_b64_e32 v[18:19], v[34:35]
	v_mad_u32_u24 v52, v164, s0, 0
	v_add3_u32 v1, v1, v148, 0
	v_mov_b32_e32 v53, 0xe0ad78ec
	s_mov_b32 s3, 8
	v_mov_b64_e32 v[4:5], v[36:37]
	v_mov_b64_e32 v[6:7], v[38:39]
	v_mov_b64_e32 v[8:9], v[40:41]
	v_mov_b64_e32 v[10:11], v[42:43]
	v_mov_b64_e32 v[12:13], v[44:45]
	v_mov_b64_e32 v[14:15], v[46:47]
	v_mov_b64_e32 v[16:17], v[48:49]
	v_mov_b64_e32 v[20:21], v[36:37]
	v_mov_b64_e32 v[22:23], v[38:39]
	v_mov_b64_e32 v[24:25], v[40:41]
	v_mov_b64_e32 v[26:27], v[42:43]
	v_mov_b64_e32 v[28:29], v[44:45]
	v_mov_b64_e32 v[30:31], v[46:47]
	v_mov_b64_e32 v[32:33], v[48:49]
	v_add_u32_e32 v246, v52, v134
	ds_read_b128 v[236:239], v246
	ds_read_b128 v[240:243], v246 offset:32
	s_branch .LBB0_969
.LBB0_968:
	v_pk_add_f32 v[220:221], v[36:37], v[52:53] op_sel:[0,1] op_sel_hi:[1,1] neg_lo:[0,1] neg_hi:[0,1]
	v_pk_add_f32 v[222:223], v[38:39], v[52:53] op_sel:[0,1] op_sel_hi:[1,1] neg_lo:[0,1] neg_hi:[0,1]
	v_pk_add_f32 v[224:225], v[40:41], v[52:53] op_sel:[0,1] op_sel_hi:[1,1] neg_lo:[0,1] neg_hi:[0,1]
	v_pk_add_f32 v[226:227], v[42:43], v[52:53] op_sel:[0,1] op_sel_hi:[1,1] neg_lo:[0,1] neg_hi:[0,1]
	v_pk_add_f32 v[228:229], v[44:45], v[52:53] op_sel:[0,1] op_sel_hi:[1,1] neg_lo:[0,1] neg_hi:[0,1]
	v_pk_add_f32 v[230:231], v[46:47], v[52:53] op_sel:[0,1] op_sel_hi:[1,1] neg_lo:[0,1] neg_hi:[0,1]
	v_pk_add_f32 v[232:233], v[48:49], v[52:53] op_sel:[0,1] op_sel_hi:[1,1] neg_lo:[0,1] neg_hi:[0,1]
	v_pk_add_f32 v[234:235], v[50:51], v[52:53] op_sel:[0,1] op_sel_hi:[1,1] neg_lo:[0,1] neg_hi:[0,1]
	v_add_u32_e32 v52, 0x1200, v52
	v_add_u32_e32 v246, v52, v134
	ds_read_b128 v[236:239], v246
	ds_read_b128 v[240:243], v246 offset:32
	v_exp_f32_e32 v201, v221
	v_exp_f32_e32 v202, v222
	v_exp_f32_e32 v203, v223
	v_exp_f32_e32 v204, v224
	v_exp_f32_e32 v205, v225
	v_exp_f32_e32 v206, v226
	v_exp_f32_e32 v207, v227
	v_add_u32_e32 v69, v1, v134
	v_exp_f32_e32 v200, v220
	v_exp_f32_e32 v208, v228
	ds_read_b64_tr_b16 v[40:41], v69 offset:55296
	ds_read_b64_tr_b16 v[42:43], v69 offset:55808
	v_exp_f32_e32 v209, v229
	v_add_u32_e32 v245, 0x6000, v69
	v_exp_f32_e32 v210, v230
	ds_read_b64_tr_b16 v[44:45], v245 offset:55296
	ds_read_b64_tr_b16 v[46:47], v245 offset:55808
	ds_read_b64_tr_b16 v[54:55], v69 offset:56320
	ds_read_b64_tr_b16 v[56:57], v69 offset:56832
	v_exp_f32_e32 v211, v231
	v_exp_f32_e32 v212, v232
	v_cvt_pk_bf16_f32 v36, v200, v201
	v_cvt_pk_bf16_f32 v37, v202, v203
	v_cvt_pk_bf16_f32 v38, v204, v205
	v_cvt_pk_bf16_f32 v39, v206, v207
	s_waitcnt lgkmcnt(4)
	v_mfma_f32_32x32x16_bf16 v[18:33], v[40:43], v[36:39], v[18:33]
	v_exp_f32_e32 v213, v233
	ds_read_b64_tr_b16 v[40:41], v245 offset:56320
	ds_read_b64_tr_b16 v[42:43], v245 offset:56832
	s_waitcnt lgkmcnt(4)
	v_mfma_f32_32x32x16_bf16 v[2:17], v[44:47], v[36:39], v[2:17]
	v_exp_f32_e32 v214, v234
	v_exp_f32_e32 v215, v235
	v_cvt_pk_bf16_f32 v36, v208, v209
	v_cvt_pk_bf16_f32 v37, v210, v211
	v_cvt_pk_bf16_f32 v38, v212, v213
	v_cvt_pk_bf16_f32 v39, v214, v215
	s_waitcnt lgkmcnt(2)
	v_mfma_f32_32x32x16_bf16 v[18:33], v[54:57], v[36:39], v[18:33]
	s_add_i32 s3, s3, -1
	s_waitcnt lgkmcnt(0)
	v_mfma_f32_32x32x16_bf16 v[2:17], v[40:43], v[36:39], v[2:17]
	v_pk_add_f32 v[220:221], v[200:201], v[202:203]
	v_pk_add_f32 v[222:223], v[204:205], v[206:207]
	v_pk_add_f32 v[224:225], v[208:209], v[210:211]
	v_pk_add_f32 v[226:227], v[212:213], v[214:215]
	v_pk_add_f32 v[220:221], v[220:221], v[222:223]
	v_pk_add_f32 v[224:225], v[224:225], v[226:227]
	v_pk_add_f32 v[220:221], v[220:221], v[224:225]
	v_add_f32_e32 v220, v220, v221
	v_add_f32_e32 v34, v34, v220
	v_add_u32_e32 v1, 0x800, v1
	s_cmp_lg_u32 s3, 0
	s_cbranch_scc0 .LBB0_971
.LBB0_969:
	v_add_u32_e32 v35, v52, v134
	s_waitcnt vmcnt(5) lgkmcnt(1)
	v_mfma_f32_32x32x16_bf16 v[36:51], v[236:239], v[82:85], 0
	s_waitcnt lgkmcnt(0)
	v_mfma_f32_32x32x16_bf16 v[36:51], v[240:243], v[74:77], v[36:51]
	ds_read_b128 v[54:57], v35 offset:64
	ds_read_b128 v[58:61], v35 offset:96
	s_waitcnt lgkmcnt(1)
	v_mfma_f32_32x32x16_bf16 v[36:51], v[54:57], v[78:81], v[36:51]
	s_waitcnt vmcnt(4) lgkmcnt(0)
	v_mfma_f32_32x32x16_bf16 v[36:51], v[58:61], v[102:105], v[36:51]
	s_nop 11
	v_max3_f32 v35, v36, v37, v38
	v_max3_f32 v54, v39, v40, v41
	v_max3_f32 v55, v42, v43, v44
	v_max3_f32 v56, v45, v46, v47
	v_max3_f32 v57, v48, v49, v50
	v_max3_f32 v35, v35, v54, v51
	v_max3_f32 v55, v55, v56, v57
	v_max_f32_e32 v35, v35, v55
	v_mov_b32_e32 v54, v35
	s_nop 1
	v_permlane32_swap_b32_e32 v35, v54
	v_max_f32_e32 v35, v35, v54
	v_add_f32_e32 v54, 0x41000000, v53
	v_cmp_gt_f32_e32 vcc, v35, v54
	s_cbranch_vccz .LBB0_968
	v_max_f32_e32 v35, v35, v35
	v_max_f32_e32 v54, v53, v53
	v_max_f32_e32 v35, v54, v35
	v_sub_f32_e32 v53, v53, v35
	v_exp_f32_e32 v54, v53
	v_mov_b32_e32 v53, v35
	v_pk_mul_f32 v[32:33], v[32:33], v[54:55] op_sel_hi:[1,0]
	v_pk_mul_f32 v[30:31], v[30:31], v[54:55] op_sel_hi:[1,0]
	v_pk_mul_f32 v[28:29], v[28:29], v[54:55] op_sel_hi:[1,0]
	v_pk_mul_f32 v[26:27], v[26:27], v[54:55] op_sel_hi:[1,0]
	v_pk_mul_f32 v[24:25], v[24:25], v[54:55] op_sel_hi:[1,0]
	v_pk_mul_f32 v[22:23], v[22:23], v[54:55] op_sel_hi:[1,0]
	v_pk_mul_f32 v[20:21], v[20:21], v[54:55] op_sel_hi:[1,0]
	v_pk_mul_f32 v[18:19], v[18:19], v[54:55] op_sel_hi:[1,0]
	v_pk_mul_f32 v[16:17], v[16:17], v[54:55] op_sel_hi:[1,0]
	v_pk_mul_f32 v[14:15], v[14:15], v[54:55] op_sel_hi:[1,0]
	v_pk_mul_f32 v[12:13], v[12:13], v[54:55] op_sel_hi:[1,0]
	v_pk_mul_f32 v[10:11], v[10:11], v[54:55] op_sel_hi:[1,0]
	v_pk_mul_f32 v[8:9], v[8:9], v[54:55] op_sel_hi:[1,0]
	v_pk_mul_f32 v[6:7], v[6:7], v[54:55] op_sel_hi:[1,0]
	v_pk_mul_f32 v[4:5], v[4:5], v[54:55] op_sel_hi:[1,0]
	v_pk_mul_f32 v[2:3], v[2:3], v[54:55] op_sel_hi:[1,0]
	v_mul_f32_e32 v34, v34, v54
	s_branch .LBB0_968
